# attention: packed f32 VALU ops with SGPR operands (ALiBi bias fma/add) split into scalar v_fma/v_add pairs
# speedup vs baseline: 1.0040x; 1.0040x over previous
; template <int MODE> ...
;     ...
;         const int dist0 = (MODE == 0) ? (t - 31 - 1024 * bcur - 64 * hi) : (t - 64 * bcur - 4 * hi);
;         float nbl = -slope2 * (float)dist0;
;         if (MODE == 1) { const unsigned mw = selw[bcur >> 5]; if (!((mw >> (bcur & 31)) & 1u)) nbl = -__builtin_inff(); }
; #pragma unroll
;         for (int r = 0; r < 16; ++r) { const float c0 = ks * (float)((r & 3) + 8 * (r >> 2)), c1 = c0 + 32.f * ks; p0[r] = fmaf(slope2, c0, p0[r]); p1[r] = fmaf(slope2, c1, p1[r]); }
;         if (bcur >= bA || bcur == bB) {
;             const float base = (float)dist0;
; #pragma unroll
;             for (int r = 0; r < 16; ++r) { const float c0 = ks * (float)((r & 3) + 8 * (r >> 2)), c1 = c0 + 32.f * ks; const float d0 = base - c0, d1 = base - c1;
;                 bool v0 = d0 >= 0.f, v1 = d1 >= 0.f;
;                 if (MODE == 2) { v0 = v0 && (d0 < 512.f); v1 = v1 && (d1 < 512.f); }
;                 p0[r] = v0 ? p0[r] : -__builtin_inff(); p1[r] = v1 ? p1[r] : -__builtin_inff(); }
.LBB0_568:
	s_mov_b32 s10, 0x43c00000
	s_mov_b32 s11, 0x43c80000
	s_nop 5
	v_fma_f32 v48, v134, s10, v16
	v_fma_f32 v49, v134, s11, v17
	s_mov_b32 s10, 0x44600000
	s_mov_b32 s11, 0x44640000
	s_lshl_b32 s7, s67, 2
	v_fma_f32 v32, v134, s10, v32
	v_fma_f32 v33, v134, s11, v33
	s_mov_b32 s10, 0x43d00000
	s_add_i32 s7, s7, -1
	s_mov_b32 s11, 0x43d80000
	s_ashr_i32 s22, s7, 6
	v_lshlrev_b32_e32 v2, 6, v170
	s_lshl_b32 s7, s6, 10
	v_fma_f32 v50, v134, s10, v18
	v_fma_f32 v51, v134, s11, v19
	s_mov_b32 s10, 0x44680000
	v_sub_u32_e32 v2, v166, v2
	s_mov_b32 s11, 0x446c0000
	s_cmp_lt_i32 s6, s22
	v_subrev_u32_e32 v179, 31, v2
	v_fma_f32 v34, v134, s10, v34
	v_fma_f32 v35, v134, s11, v35
	s_cselect_b64 s[10:11], -1, 0
	s_cmp_lg_u32 s6, -1
	s_barrier
	v_subrev_u32_e32 v2, s7, v179
	s_cselect_b64 s[6:7], -1, 0
	s_and_b64 s[6:7], s[10:11], s[6:7]
	v_fma_f32 v36, v134, s64, v4
	v_fma_f32 v37, v134, s65, v5
	v_fma_f32 v20, v134, s82, v20
	v_fma_f32 v21, v134, s83, v21
	v_fma_f32 v38, v134, s60, v6
	v_fma_f32 v39, v134, s61, v7
	v_fma_f32 v22, v134, s38, v22
	v_fma_f32 v23, v134, s39, v23
	v_fma_f32 v40, v134, s40, v8
	v_fma_f32 v41, v134, s41, v9
	v_fma_f32 v24, v134, s42, v24
	v_fma_f32 v25, v134, s43, v25
	v_fma_f32 v42, v134, s44, v10
	v_fma_f32 v43, v134, s45, v11
	v_fma_f32 v26, v134, s46, v26
	v_fma_f32 v27, v134, s47, v27
	v_fma_f32 v44, v134, s48, v12
	v_fma_f32 v45, v134, s49, v13
	v_fma_f32 v28, v134, s50, v28
	v_fma_f32 v29, v134, s51, v29
	v_fma_f32 v46, v134, s62, v14
	v_fma_f32 v47, v134, s63, v15
	v_fma_f32 v30, v134, s58, v30
	v_fma_f32 v31, v134, s59, v31
	s_and_b64 vcc, exec, s[6:7]
	s_cbranch_vccnz .LBB0_570
	v_cmp_lt_i32_e32 vcc, -1, v2
	s_nop 1
	v_cndmask_b32_e32 v36, v161, v36, vcc
	v_cmp_lt_i32_e32 vcc, 15, v2
	s_nop 1
	v_cndmask_b32_e32 v37, v161, v37, vcc
	v_cmp_lt_i32_e32 vcc, 31, v2
	s_nop 1
	v_cndmask_b32_e32 v38, v161, v38, vcc
	v_cmp_lt_i32_e32 vcc, 47, v2
	s_nop 1
	v_cndmask_b32_e32 v39, v161, v39, vcc
	v_cmp_lt_i32_e32 vcc, s36, v2
	s_nop 1
	v_cndmask_b32_e32 v40, v161, v40, vcc
	v_cmp_lt_i32_e32 vcc, s66, v2
	s_nop 1
	v_cndmask_b32_e32 v41, v161, v41, vcc
	v_cmp_lt_i32_e32 vcc, s77, v2
	s_nop 1
	v_cndmask_b32_e32 v42, v161, v42, vcc
	v_cmp_lt_i32_e32 vcc, s76, v2
	s_nop 1
	v_cndmask_b32_e32 v43, v161, v43, vcc
	v_cmp_lt_i32_e32 vcc, s5, v2
	s_nop 1
	v_cndmask_b32_e32 v44, v161, v44, vcc
	v_cmp_lt_i32_e32 vcc, s4, v2
	s_nop 1
	v_cndmask_b32_e32 v45, v161, v45, vcc
	v_cmp_lt_i32_e32 vcc, s73, v2
	s_nop 1
	v_cndmask_b32_e32 v46, v161, v46, vcc
	v_cmp_lt_i32_e32 vcc, s74, v2
	s_nop 1
	v_cndmask_b32_e32 v47, v161, v47, vcc
	v_cmp_lt_i32_e32 vcc, s26, v2
	s_nop 1
	v_cndmask_b32_e32 v48, v161, v48, vcc
	v_cmp_lt_i32_e32 vcc, s27, v2
	s_nop 1
	v_cndmask_b32_e32 v49, v161, v49, vcc
	v_cmp_lt_i32_e32 vcc, s28, v2
	s_nop 1
	v_cndmask_b32_e32 v50, v161, v50, vcc
	v_cmp_lt_i32_e32 vcc, s37, v2
	s_nop 1
	v_cndmask_b32_e32 v51, v161, v51, vcc
	v_cmp_lt_i32_e32 vcc, s33, v2
	s_nop 1
	v_cndmask_b32_e32 v20, v161, v20, vcc
	v_cmp_lt_i32_e32 vcc, s89, v2
	s_nop 1
	v_cndmask_b32_e32 v21, v161, v21, vcc
	v_cmp_lt_i32_e32 vcc, s88, v2
	s_nop 1
	v_cndmask_b32_e32 v22, v161, v22, vcc
	v_cmp_lt_i32_e32 vcc, s93, v2
	s_nop 1
	v_cndmask_b32_e32 v23, v161, v23, vcc
	v_cmp_lt_i32_e32 vcc, s92, v2
	s_nop 1
	v_cndmask_b32_e32 v24, v161, v24, vcc
	v_cmp_lt_i32_e32 vcc, s87, v2
	s_nop 1
	v_cndmask_b32_e32 v25, v161, v25, vcc
	v_cmp_lt_i32_e32 vcc, s86, v2
	s_nop 1
	v_cndmask_b32_e32 v26, v161, v26, vcc
	v_cmp_lt_i32_e32 vcc, s0, v2
	s_nop 1
	v_cndmask_b32_e32 v27, v161, v27, vcc
	v_cmp_lt_i32_e32 vcc, s81, v2
	s_nop 1
	v_cndmask_b32_e32 v28, v161, v28, vcc
	v_cmp_lt_i32_e32 vcc, s80, v2
	s_nop 1
	v_cndmask_b32_e32 v29, v161, v29, vcc
	v_cmp_lt_i32_e32 vcc, s79, v2
	s_nop 1
	v_cndmask_b32_e32 v30, v161, v30, vcc
	v_cmp_lt_i32_e32 vcc, s78, v2
	s_nop 1
	v_cndmask_b32_e32 v31, v161, v31, vcc
	v_cmp_lt_i32_e32 vcc, s71, v2
	s_nop 1
	v_cndmask_b32_e32 v32, v161, v32, vcc
	v_cmp_lt_i32_e32 vcc, s70, v2
	s_nop 1
	v_cndmask_b32_e32 v33, v161, v33, vcc
	v_cmp_lt_i32_e32 vcc, s69, v2
	s_nop 1
	v_cndmask_b32_e32 v34, v161, v34, vcc
	v_cmp_lt_i32_e32 vcc, s68, v2
	s_nop 1
	v_cndmask_b32_e32 v35, v161, v35, vcc

; template <int MODE> ...
;     ...
;         for (int r = 0; r < 16; ++r) { const float c0 = ks * (float)((r & 3) + 8 * (r >> 2)), c1 = c0 + 32.f * ks; p0[r] = fmaf(slope2, c0, p0[r]); p1[r] = fmaf(slope2, c1, p1[r]); }
;         if (bcur >= bA || bcur == bB) {
;             const float base = (float)dist0;
; #pragma unroll
;             for (int r = 0; r < 16; ++r) { const float c0 = ks * (float)((r & 3) + 8 * (r >> 2)), c1 = c0 + 32.f * ks; const float d0 = base - c0, d1 = base - c1;
;                 bool v0 = d0 >= 0.f, v1 = d1 >= 0.f;
;                 if (MODE == 2) { v0 = v0 && (d0 < 512.f); v1 = v1 && (d1 < 512.f); }
;                 p0[r] = v0 ? p0[r] : -__builtin_inff(); p1[r] = v1 ? p1[r] : -__builtin_inff(); }
.LBB0_583:
	s_lshl_b32 s16, s26, 10
	v_subrev_u32_e32 v181, s16, v179
	s_mov_b32 s16, 0x43c00000
	s_mov_b32 s17, 0x43c80000
	v_fma_f32 v144, v134, s64, v68
	v_fma_f32 v145, v135, s65, v69
	v_fma_f32 v68, v134, s82, v84
	v_fma_f32 v69, v135, s83, v85
	v_fma_f32 v84, v134, s60, v70
	v_fma_f32 v85, v135, s61, v71
	v_fma_f32 v70, v134, s38, v86
	v_fma_f32 v71, v135, s39, v87
	v_fma_f32 v86, v134, s40, v72
	v_fma_f32 v87, v135, s41, v73
	v_fma_f32 v72, v134, s42, v88
	v_fma_f32 v73, v135, s43, v89
	v_fma_f32 v88, v134, s44, v74
	v_fma_f32 v89, v135, s45, v75
	v_fma_f32 v74, v134, s46, v90
	v_fma_f32 v75, v135, s47, v91
	v_fma_f32 v90, v134, s48, v76
	v_fma_f32 v91, v135, s49, v77
	v_fma_f32 v76, v134, s50, v92
	v_fma_f32 v77, v135, s51, v93
	v_fma_f32 v92, v134, s62, v78
	v_fma_f32 v93, v135, s63, v79
	v_fma_f32 v78, v134, s58, v94
	v_fma_f32 v79, v135, s59, v95
	v_fma_f32 v94, v134, s16, v80
	v_fma_f32 v95, v135, s17, v81
	s_mov_b32 s16, 0x44600000
	s_mov_b32 s17, 0x44640000
	v_fma_f32 v80, v134, s16, v96
	v_fma_f32 v81, v135, s17, v97
	s_mov_b32 s16, 0x43d00000
	s_mov_b32 s17, 0x43d80000
	v_fma_f32 v96, v134, s16, v82
	v_fma_f32 v97, v135, s17, v83
	s_mov_b32 s16, 0x44680000
	s_mov_b32 s17, 0x446c0000
	s_cmp_lt_i32 s26, s22
	v_fma_f32 v82, v134, s16, v98
	v_fma_f32 v83, v135, s17, v99
	s_cselect_b64 s[16:17], -1, 0
	s_cmp_lg_u32 s26, -1
	s_cselect_b64 s[24:25], -1, 0
	s_and_b64 s[16:17], s[16:17], s[24:25]
	s_and_b64 vcc, exec, s[16:17]
	s_cbranch_vccnz .LBB0_586
	v_cmp_lt_i32_e32 vcc, -1, v181
	s_movk_i32 s16, 0x17f
	s_movk_i32 s28, 0x19f
	v_cndmask_b32_e32 v144, v161, v144, vcc
	v_cmp_lt_i32_e32 vcc, 15, v181
	s_nop 1
	v_cndmask_b32_e32 v145, v161, v145, vcc
	v_cmp_lt_i32_e32 vcc, 31, v181
	s_nop 1
	v_cndmask_b32_e32 v84, v161, v84, vcc
	v_cmp_lt_i32_e32 vcc, 47, v181
	s_nop 1
	v_cndmask_b32_e32 v85, v161, v85, vcc
	v_cmp_lt_i32_e32 vcc, s36, v181
	s_nop 1
	v_cndmask_b32_e32 v86, v161, v86, vcc
	v_cmp_lt_i32_e32 vcc, s66, v181
	s_nop 1
	v_cndmask_b32_e32 v87, v161, v87, vcc
	v_cmp_lt_i32_e32 vcc, s77, v181
	s_nop 1
	v_cndmask_b32_e32 v88, v161, v88, vcc
	v_cmp_lt_i32_e32 vcc, s76, v181
	s_nop 1
	v_cndmask_b32_e32 v89, v161, v89, vcc
	v_cmp_lt_i32_e32 vcc, s5, v181
	s_nop 1
	v_cndmask_b32_e32 v90, v161, v90, vcc
	v_cmp_lt_i32_e32 vcc, s4, v181
	s_nop 1
	v_cndmask_b32_e32 v91, v161, v91, vcc
	v_cmp_lt_i32_e32 vcc, s73, v181
	s_nop 1
	v_cndmask_b32_e32 v92, v161, v92, vcc
	v_cmp_lt_i32_e32 vcc, s74, v181
	s_nop 1
	v_cndmask_b32_e32 v93, v161, v93, vcc
	v_cmp_lt_i32_e32 vcc, s16, v181
	s_nop 1
	v_cndmask_b32_e32 v94, v161, v94, vcc
	v_cmp_lt_i32_e32 vcc, s27, v181
	s_nop 1
	v_cndmask_b32_e32 v95, v161, v95, vcc
	v_cmp_lt_i32_e32 vcc, s28, v181
	s_nop 1
	v_cndmask_b32_e32 v96, v161, v96, vcc
	v_cmp_lt_i32_e32 vcc, s37, v181
	s_nop 1
	v_cndmask_b32_e32 v97, v161, v97, vcc
	v_cmp_lt_i32_e32 vcc, s33, v181
	s_nop 1
	v_cndmask_b32_e32 v68, v161, v68, vcc
	v_cmp_lt_i32_e32 vcc, s89, v181
	s_nop 1
	v_cndmask_b32_e32 v69, v161, v69, vcc
	v_cmp_lt_i32_e32 vcc, s88, v181
	s_nop 1
	v_cndmask_b32_e32 v70, v161, v70, vcc
	v_cmp_lt_i32_e32 vcc, s93, v181
	s_nop 1
	v_cndmask_b32_e32 v71, v161, v71, vcc
	v_cmp_lt_i32_e32 vcc, s92, v181
	s_nop 1
	v_cndmask_b32_e32 v72, v161, v72, vcc
	v_cmp_lt_i32_e32 vcc, s87, v181
	s_nop 1
	v_cndmask_b32_e32 v73, v161, v73, vcc
	v_cmp_lt_i32_e32 vcc, s86, v181
	s_nop 1
	v_cndmask_b32_e32 v74, v161, v74, vcc
	v_cmp_lt_i32_e32 vcc, s0, v181
	s_nop 1
	v_cndmask_b32_e32 v75, v161, v75, vcc
	v_cmp_lt_i32_e32 vcc, s81, v181
	s_nop 1
	v_cndmask_b32_e32 v76, v161, v76, vcc
	v_cmp_lt_i32_e32 vcc, s80, v181
	s_nop 1
	v_cndmask_b32_e32 v77, v161, v77, vcc
	v_cmp_lt_i32_e32 vcc, s79, v181
	s_nop 1
	v_cndmask_b32_e32 v78, v161, v78, vcc
	v_cmp_lt_i32_e32 vcc, s78, v181
	s_nop 1
	v_cndmask_b32_e32 v79, v161, v79, vcc
	v_cmp_lt_i32_e32 vcc, s71, v181
	s_nop 1
	v_cndmask_b32_e32 v80, v161, v80, vcc
	v_cmp_lt_i32_e32 vcc, s70, v181
	s_nop 1
	v_cndmask_b32_e32 v81, v161, v81, vcc
	v_cmp_lt_i32_e32 vcc, s69, v181
	s_nop 1
	v_cndmask_b32_e32 v82, v161, v82, vcc
	v_cmp_lt_i32_e32 vcc, s68, v181
	s_nop 1
	v_cndmask_b32_e32 v83, v161, v83, vcc
	s_branch .LBB0_587

; template <int MODE> ...
;     ...
;         for (int r = 0; r < 16; ++r) { const float c0 = ks * (float)((r & 3) + 8 * (r >> 2)), c1 = c0 + 32.f * ks; p0[r] = fmaf(slope2, c0, p0[r]); p1[r] = fmaf(slope2, c1, p1[r]); }
;         if (bcur >= bA || bcur == bB) {
;             const float base = (float)dist0;
; #pragma unroll
;             for (int r = 0; r < 16; ++r) { const float c0 = ks * (float)((r & 3) + 8 * (r >> 2)), c1 = c0 + 32.f * ks; const float d0 = base - c0, d1 = base - c1;
;                 bool v0 = d0 >= 0.f, v1 = d1 >= 0.f;
;                 if (MODE == 2) { v0 = v0 && (d0 < 512.f); v1 = v1 && (d1 < 512.f); }
;                 p0[r] = v0 ? p0[r] : -__builtin_inff(); p1[r] = v1 ? p1[r] : -__builtin_inff(); }
.LBB0_604:
	s_mov_b32 s34, 0x43c00000
	s_mov_b32 s35, 0x43c80000
	s_nop 2
	v_fma_f32 v144, v134, s64, v68
	v_fma_f32 v145, v135, s65, v69
	s_nop 1
	v_fma_f32 v68, v134, s82, v84
	v_fma_f32 v69, v135, s83, v85
	v_fma_f32 v84, v134, s60, v70
	v_fma_f32 v85, v135, s61, v71
	v_fma_f32 v70, v134, s38, v86
	v_fma_f32 v71, v135, s39, v87
	v_fma_f32 v86, v134, s40, v72
	v_fma_f32 v87, v135, s41, v73
	v_fma_f32 v72, v134, s42, v88
	v_fma_f32 v73, v135, s43, v89
	v_fma_f32 v88, v134, s44, v74
	v_fma_f32 v89, v135, s45, v75
	v_fma_f32 v74, v134, s46, v90
	v_fma_f32 v75, v135, s47, v91
	v_fma_f32 v90, v134, s48, v76
	v_fma_f32 v91, v135, s49, v77
	v_fma_f32 v76, v134, s50, v92
	v_fma_f32 v77, v135, s51, v93
	v_fma_f32 v92, v134, s62, v78
	v_fma_f32 v93, v135, s63, v79
	v_fma_f32 v78, v134, s58, v94
	v_fma_f32 v79, v135, s59, v95
	v_fma_f32 v94, v134, s34, v80
	v_fma_f32 v95, v135, s35, v81
	s_mov_b32 s34, 0x44600000
	s_mov_b32 s35, 0x44640000
	v_fma_f32 v80, v134, s34, v96
	v_fma_f32 v81, v135, s35, v97
	s_mov_b32 s34, 0x43d00000
	s_mov_b32 s35, 0x43d80000
	s_lshl_b32 s17, s16, 10
	v_fma_f32 v96, v134, s34, v82
	v_fma_f32 v97, v135, s35, v83
	s_mov_b32 s34, 0x44680000
	s_mov_b32 s35, 0x446c0000
	s_cmp_lt_i32 s16, s22
	v_fma_f32 v82, v134, s34, v98
	v_fma_f32 v83, v135, s35, v99
	s_cselect_b64 s[34:35], -1, 0
	s_cmp_lg_u32 s16, -1
	v_subrev_u32_e32 v175, s17, v179
	s_cselect_b64 s[16:17], -1, 0
	s_and_b64 s[16:17], s[34:35], s[16:17]
	s_and_b64 vcc, exec, s[16:17]
	s_cbranch_vccnz .LBB0_606
	v_cmp_lt_i32_e32 vcc, -1, v175
	s_nop 1
	v_cndmask_b32_e32 v144, v161, v144, vcc
	v_cmp_lt_i32_e32 vcc, 15, v175
	s_nop 1
	v_cndmask_b32_e32 v145, v161, v145, vcc
	v_cmp_lt_i32_e32 vcc, 31, v175
	s_nop 1
	v_cndmask_b32_e32 v84, v161, v84, vcc
	v_cmp_lt_i32_e32 vcc, 47, v175
	s_nop 1
	v_cndmask_b32_e32 v85, v161, v85, vcc
	v_cmp_lt_i32_e32 vcc, s36, v175
	s_nop 1
	v_cndmask_b32_e32 v86, v161, v86, vcc
	v_cmp_lt_i32_e32 vcc, s66, v175
	s_nop 1
	v_cndmask_b32_e32 v87, v161, v87, vcc
	v_cmp_lt_i32_e32 vcc, s77, v175
	s_nop 1
	v_cndmask_b32_e32 v88, v161, v88, vcc
	v_cmp_lt_i32_e32 vcc, s76, v175
	s_nop 1
	v_cndmask_b32_e32 v89, v161, v89, vcc
	v_cmp_lt_i32_e32 vcc, s5, v175
	s_nop 1
	v_cndmask_b32_e32 v90, v161, v90, vcc
	v_cmp_lt_i32_e32 vcc, s4, v175
	s_nop 1
	v_cndmask_b32_e32 v91, v161, v91, vcc
	v_cmp_lt_i32_e32 vcc, s73, v175
	s_nop 1
	v_cndmask_b32_e32 v92, v161, v92, vcc
	v_cmp_lt_i32_e32 vcc, s74, v175
	s_nop 1
	v_cndmask_b32_e32 v93, v161, v93, vcc
	v_cmp_lt_i32_e32 vcc, s54, v175
	s_nop 1
	v_cndmask_b32_e32 v94, v161, v94, vcc
	v_cmp_lt_i32_e32 vcc, s53, v175
	s_nop 1
	v_cndmask_b32_e32 v95, v161, v95, vcc
	v_cmp_lt_i32_e32 vcc, s52, v175
	s_nop 1
	v_cndmask_b32_e32 v96, v161, v96, vcc
	v_cmp_lt_i32_e32 vcc, s37, v175
	s_nop 1
	v_cndmask_b32_e32 v97, v161, v97, vcc
	v_cmp_lt_i32_e32 vcc, s33, v175
	s_nop 1
	v_cndmask_b32_e32 v68, v161, v68, vcc
	v_cmp_lt_i32_e32 vcc, s89, v175
	s_nop 1
	v_cndmask_b32_e32 v69, v161, v69, vcc
	v_cmp_lt_i32_e32 vcc, s88, v175
	s_nop 1
	v_cndmask_b32_e32 v70, v161, v70, vcc
	v_cmp_lt_i32_e32 vcc, s93, v175
	s_nop 1
	v_cndmask_b32_e32 v71, v161, v71, vcc
	v_cmp_lt_i32_e32 vcc, s92, v175
	s_nop 1
	v_cndmask_b32_e32 v72, v161, v72, vcc
	v_cmp_lt_i32_e32 vcc, s87, v175
	s_nop 1
	v_cndmask_b32_e32 v73, v161, v73, vcc
	v_cmp_lt_i32_e32 vcc, s86, v175
	s_nop 1
	v_cndmask_b32_e32 v74, v161, v74, vcc
	v_cmp_lt_i32_e32 vcc, s0, v175
	s_nop 1
	v_cndmask_b32_e32 v75, v161, v75, vcc
	v_cmp_lt_i32_e32 vcc, s81, v175
	s_nop 1
	v_cndmask_b32_e32 v76, v161, v76, vcc
	v_cmp_lt_i32_e32 vcc, s80, v175
	s_nop 1
	v_cndmask_b32_e32 v77, v161, v77, vcc
	v_cmp_lt_i32_e32 vcc, s79, v175
	s_nop 1
	v_cndmask_b32_e32 v78, v161, v78, vcc
	v_cmp_lt_i32_e32 vcc, s78, v175
	s_nop 1
	v_cndmask_b32_e32 v79, v161, v79, vcc
	v_cmp_lt_i32_e32 vcc, s71, v175
	s_nop 1
	v_cndmask_b32_e32 v80, v161, v80, vcc
	v_cmp_lt_i32_e32 vcc, s70, v175
	s_nop 1
	v_cndmask_b32_e32 v81, v161, v81, vcc
	v_cmp_lt_i32_e32 vcc, s69, v175
	s_nop 1
	v_cndmask_b32_e32 v82, v161, v82, vcc
	v_cmp_lt_i32_e32 vcc, s68, v175
	s_nop 1
	v_cndmask_b32_e32 v83, v161, v83, vcc

; template <int MODE> ...
;     ...
;         const int dist0 = (MODE == 0) ? (t - 31 - 1024 * bcur - 64 * hi) : (t - 64 * bcur - 4 * hi);
;         float nbl = -slope2 * (float)dist0;
;         if (MODE == 1) { const unsigned mw = selw[bcur >> 5]; if (!((mw >> (bcur & 31)) & 1u)) nbl = -__builtin_inff(); }
; #pragma unroll
;         for (int r = 0; r < 16; ++r) { const float c0 = ks * (float)((r & 3) + 8 * (r >> 2)), c1 = c0 + 32.f * ks; p0[r] = fmaf(slope2, c0, p0[r]); p1[r] = fmaf(slope2, c1, p1[r]); }
;         if (bcur >= bA || bcur == bB) {
;             const float base = (float)dist0;
; #pragma unroll
;             for (int r = 0; r < 16; ++r) { const float c0 = ks * (float)((r & 3) + 8 * (r >> 2)), c1 = c0 + 32.f * ks; const float d0 = base - c0, d1 = base - c1;
;                 bool v0 = d0 >= 0.f, v1 = d1 >= 0.f;
;                 if (MODE == 2) { v0 = v0 && (d0 < 512.f); v1 = v1 && (d1 < 512.f); }
;                 p0[r] = v0 ? p0[r] : -__builtin_inff(); p1[r] = v1 ? p1[r] : -__builtin_inff(); }
.LBB0_746:
	s_add_i32 s9, 0, 0x20c00
	v_lshl_add_u32 v172, v172, 4, s9
	s_ashr_i32 s9, s8, 5
	s_barrier
	v_lshl_add_u32 v36, s9, 2, v172
	ds_read_b32 v52, v36
	s_cmp_lt_i32 s8, s67
	s_cselect_b64 s[16:17], -1, 0
	s_cmp_lg_u32 s8, -1
	s_cselect_b64 s[18:19], -1, 0
	v_lshl_add_u32 v2, s8, 6, v140
	s_mov_b32 s84, s60
	s_mov_b32 s94, s65
	s_mov_b32 s74, s61
	s_and_b64 s[16:17], s[16:17], s[18:19]
	v_sub_u32_e32 v2, v166, v2
	v_fma_f32 v51, 0, v134, v4
	v_add_f32_e32 v50, v134, v5
	v_fma_f32 v20, v134, s84, v20
	v_fma_f32 v21, v134, s85, v21
	v_fma_f32 v36, v134, s22, v6
	v_fma_f32 v37, v134, s23, v7
	v_fma_f32 v22, v134, s24, v22
	v_fma_f32 v23, v134, s25, v23
	v_fma_f32 v38, v134, s56, v8
	v_fma_f32 v39, v134, s57, v9
	v_fma_f32 v24, v134, s26, v24
	v_fma_f32 v25, v134, s27, v25
	v_fma_f32 v40, v134, s28, v10
	v_fma_f32 v41, v134, s29, v11
	v_fma_f32 v26, v134, s36, v26
	v_fma_f32 v27, v134, s37, v27
	v_fma_f32 v42, v134, s94, v12
	v_fma_f32 v43, v134, s95, v13
	v_fma_f32 v28, v134, s74, v28
	v_fma_f32 v29, v134, s75, v29
	v_fma_f32 v44, v134, s38, v14
	v_fma_f32 v45, v134, s39, v15
	v_fma_f32 v30, v134, s40, v30
	v_fma_f32 v31, v134, s41, v31
	v_fma_f32 v46, v134, s42, v16
	v_fma_f32 v47, v134, s43, v17
	v_fma_f32 v32, v134, s44, v32
	v_fma_f32 v33, v134, s45, v33
	v_fma_f32 v48, v134, s46, v18
	v_fma_f32 v49, v134, s47, v19
	v_fma_f32 v34, v134, s48, v34
	v_fma_f32 v35, v134, s49, v35
	s_and_b64 vcc, exec, s[16:17]
	s_cbranch_vccnz .LBB0_748
	v_cmp_lt_i32_e32 vcc, -1, v2
	s_nop 1
	v_cndmask_b32_e32 v51, v161, v51, vcc
	v_cmp_lt_i32_e32 vcc, 0, v2
	s_nop 1
	v_cndmask_b32_e32 v50, v161, v50, vcc
	v_cmp_lt_i32_e32 vcc, 1, v2
	s_nop 1
	v_cndmask_b32_e32 v36, v161, v36, vcc
	v_cmp_lt_i32_e32 vcc, 2, v2
	s_nop 1
	v_cndmask_b32_e32 v37, v161, v37, vcc
	v_cmp_lt_i32_e32 vcc, 7, v2
	s_nop 1
	v_cndmask_b32_e32 v38, v161, v38, vcc
	v_cmp_lt_i32_e32 vcc, 8, v2
	s_nop 1
	v_cndmask_b32_e32 v39, v161, v39, vcc
	v_cmp_lt_i32_e32 vcc, 9, v2
	s_nop 1
	v_cndmask_b32_e32 v40, v161, v40, vcc
	v_cmp_lt_i32_e32 vcc, 10, v2
	s_nop 1
	v_cndmask_b32_e32 v41, v161, v41, vcc
	v_cmp_lt_i32_e32 vcc, 15, v2
	s_nop 1
	v_cndmask_b32_e32 v42, v161, v42, vcc
	v_cmp_lt_i32_e32 vcc, 16, v2
	s_nop 1
	v_cndmask_b32_e32 v43, v161, v43, vcc
	v_cmp_lt_i32_e32 vcc, 17, v2
	s_nop 1
	v_cndmask_b32_e32 v44, v161, v44, vcc
	v_cmp_lt_i32_e32 vcc, 18, v2
	s_nop 1
	v_cndmask_b32_e32 v45, v161, v45, vcc
	v_cmp_lt_i32_e32 vcc, 23, v2
	s_nop 1
	v_cndmask_b32_e32 v46, v161, v46, vcc
	v_cmp_lt_i32_e32 vcc, 24, v2
	s_nop 1
	v_cndmask_b32_e32 v47, v161, v47, vcc
	v_cmp_lt_i32_e32 vcc, 25, v2
	s_nop 1
	v_cndmask_b32_e32 v48, v161, v48, vcc
	v_cmp_lt_i32_e32 vcc, 26, v2
	s_nop 1
	v_cndmask_b32_e32 v49, v161, v49, vcc
	v_cmp_lt_i32_e32 vcc, 31, v2
	s_nop 1
	v_cndmask_b32_e32 v20, v161, v20, vcc
	v_cmp_lt_i32_e32 vcc, 32, v2
	s_nop 1
	v_cndmask_b32_e32 v21, v161, v21, vcc
	v_cmp_lt_i32_e32 vcc, 33, v2
	s_nop 1
	v_cndmask_b32_e32 v22, v161, v22, vcc
	v_cmp_lt_i32_e32 vcc, 34, v2
	s_nop 1
	v_cndmask_b32_e32 v23, v161, v23, vcc
	v_cmp_lt_i32_e32 vcc, 39, v2
	s_nop 1
	v_cndmask_b32_e32 v24, v161, v24, vcc
	v_cmp_lt_i32_e32 vcc, 40, v2
	s_nop 1
	v_cndmask_b32_e32 v25, v161, v25, vcc
	v_cmp_lt_i32_e32 vcc, 41, v2
	s_nop 1
	v_cndmask_b32_e32 v26, v161, v26, vcc
	v_cmp_lt_i32_e32 vcc, 42, v2
	s_nop 1
	v_cndmask_b32_e32 v27, v161, v27, vcc
	v_cmp_lt_i32_e32 vcc, 47, v2
	s_nop 1
	v_cndmask_b32_e32 v28, v161, v28, vcc
	v_cmp_lt_i32_e32 vcc, 48, v2
	s_nop 1
	v_cndmask_b32_e32 v29, v161, v29, vcc
	v_cmp_lt_i32_e32 vcc, 49, v2
	s_nop 1
	v_cndmask_b32_e32 v30, v161, v30, vcc
	v_cmp_lt_i32_e32 vcc, 50, v2
	s_nop 1
	v_cndmask_b32_e32 v31, v161, v31, vcc
	v_cmp_lt_i32_e32 vcc, 55, v2
	s_nop 1
	v_cndmask_b32_e32 v32, v161, v32, vcc
	v_cmp_lt_i32_e32 vcc, 56, v2
	s_nop 1
	v_cndmask_b32_e32 v33, v161, v33, vcc
	v_cmp_lt_i32_e32 vcc, 57, v2
	s_nop 1
	v_cndmask_b32_e32 v34, v161, v34, vcc
	v_cmp_lt_i32_e32 vcc, 58, v2
	s_nop 1
	v_cndmask_b32_e32 v35, v161, v35, vcc

; template <int MODE> ...
;     ...
;         if (MODE == 1) { const unsigned mw = selw[bcur >> 5]; if (!((mw >> (bcur & 31)) & 1u)) nbl = -__builtin_inff(); }
; #pragma unroll
;         for (int r = 0; r < 16; ++r) { const float c0 = ks * (float)((r & 3) + 8 * (r >> 2)), c1 = c0 + 32.f * ks; p0[r] = fmaf(slope2, c0, p0[r]); p1[r] = fmaf(slope2, c1, p1[r]); }
;         if (bcur >= bA || bcur == bB) {
;             const float base = (float)dist0;
; #pragma unroll
;             for (int r = 0; r < 16; ++r) { const float c0 = ks * (float)((r & 3) + 8 * (r >> 2)), c1 = c0 + 32.f * ks; const float d0 = base - c0, d1 = base - c1;
;                 bool v0 = d0 >= 0.f, v1 = d1 >= 0.f;
;                 if (MODE == 2) { v0 = v0 && (d0 < 512.f); v1 = v1 && (d1 < 512.f); }
;                 p0[r] = v0 ? p0[r] : -__builtin_inff(); p1[r] = v1 ? p1[r] : -__builtin_inff(); }
.LBB0_760:
	v_lshl_add_u32 v183, s16, 6, v140
	s_ashr_i32 s7, s16, 5
	v_sub_u32_e32 v184, v166, v183
	v_lshl_add_u32 v183, s7, 2, v172
	ds_read_b32 v183, v183
	s_cmp_lt_i32 s16, s67
	s_cselect_b64 s[12:13], -1, 0
	s_cmp_lg_u32 s16, -1
	s_cselect_b64 s[18:19], -1, 0
	s_mov_b32 s84, s60
	s_mov_b32 s94, s65
	s_mov_b32 s74, s61
	s_and_b64 s[12:13], s[12:13], s[18:19]
	v_fma_f32 v190, 0, v134, v68
	v_add_f32_e32 v189, v134, v69
	v_fma_f32 v68, v134, s84, v84
	v_fma_f32 v69, v135, s85, v85
	v_fma_f32 v84, v134, s22, v70
	v_fma_f32 v85, v135, s23, v71
	v_fma_f32 v70, v134, s24, v86
	v_fma_f32 v71, v135, s25, v87
	v_fma_f32 v86, v134, s56, v72
	v_fma_f32 v87, v135, s57, v73
	v_fma_f32 v72, v134, s26, v88
	v_fma_f32 v73, v135, s27, v89
	v_fma_f32 v88, v134, s28, v74
	v_fma_f32 v89, v135, s29, v75
	v_fma_f32 v74, v134, s36, v90
	v_fma_f32 v75, v135, s37, v91
	v_fma_f32 v90, v134, s94, v76
	v_fma_f32 v91, v135, s95, v77
	v_fma_f32 v76, v134, s74, v92
	v_fma_f32 v77, v135, s75, v93
	v_fma_f32 v92, v134, s38, v78
	v_fma_f32 v93, v135, s39, v79
	v_fma_f32 v78, v134, s40, v94
	v_fma_f32 v79, v135, s41, v95
	v_fma_f32 v94, v134, s42, v80
	v_fma_f32 v95, v135, s43, v81
	v_fma_f32 v80, v134, s44, v96
	v_fma_f32 v81, v135, s45, v97
	v_fma_f32 v96, v134, s46, v82
	v_fma_f32 v97, v135, s47, v83
	v_fma_f32 v82, v134, s48, v98
	v_fma_f32 v83, v135, s49, v99
	s_and_b64 vcc, exec, s[12:13]
	s_cbranch_vccnz .LBB0_762
	v_cmp_lt_i32_e32 vcc, -1, v184
	s_nop 1
	v_cndmask_b32_e32 v190, v161, v190, vcc
	v_cmp_lt_i32_e32 vcc, 0, v184
	s_nop 1
	v_cndmask_b32_e32 v189, v161, v189, vcc
	v_cmp_lt_i32_e32 vcc, 1, v184
	s_nop 1
	v_cndmask_b32_e32 v84, v161, v84, vcc
	v_cmp_lt_i32_e32 vcc, 2, v184
	s_nop 1
	v_cndmask_b32_e32 v85, v161, v85, vcc
	v_cmp_lt_i32_e32 vcc, 7, v184
	s_nop 1
	v_cndmask_b32_e32 v86, v161, v86, vcc
	v_cmp_lt_i32_e32 vcc, 8, v184
	s_nop 1
	v_cndmask_b32_e32 v87, v161, v87, vcc
	v_cmp_lt_i32_e32 vcc, 9, v184
	s_nop 1
	v_cndmask_b32_e32 v88, v161, v88, vcc
	v_cmp_lt_i32_e32 vcc, 10, v184
	s_nop 1
	v_cndmask_b32_e32 v89, v161, v89, vcc
	v_cmp_lt_i32_e32 vcc, 15, v184
	s_nop 1
	v_cndmask_b32_e32 v90, v161, v90, vcc
	v_cmp_lt_i32_e32 vcc, 16, v184
	s_nop 1
	v_cndmask_b32_e32 v91, v161, v91, vcc
	v_cmp_lt_i32_e32 vcc, 17, v184
	s_nop 1
	v_cndmask_b32_e32 v92, v161, v92, vcc
	v_cmp_lt_i32_e32 vcc, 18, v184
	s_nop 1
	v_cndmask_b32_e32 v93, v161, v93, vcc
	v_cmp_lt_i32_e32 vcc, 23, v184
	s_nop 1
	v_cndmask_b32_e32 v94, v161, v94, vcc
	v_cmp_lt_i32_e32 vcc, 24, v184
	s_nop 1
	v_cndmask_b32_e32 v95, v161, v95, vcc
	v_cmp_lt_i32_e32 vcc, 25, v184
	s_nop 1
	v_cndmask_b32_e32 v96, v161, v96, vcc
	v_cmp_lt_i32_e32 vcc, 26, v184
	s_nop 1
	v_cndmask_b32_e32 v97, v161, v97, vcc
	v_cmp_lt_i32_e32 vcc, 31, v184
	s_nop 1
	v_cndmask_b32_e32 v68, v161, v68, vcc
	v_cmp_lt_i32_e32 vcc, 32, v184
	s_nop 1
	v_cndmask_b32_e32 v69, v161, v69, vcc
	v_cmp_lt_i32_e32 vcc, 33, v184
	s_nop 1
	v_cndmask_b32_e32 v70, v161, v70, vcc
	v_cmp_lt_i32_e32 vcc, 34, v184
	s_nop 1
	v_cndmask_b32_e32 v71, v161, v71, vcc
	v_cmp_lt_i32_e32 vcc, 39, v184
	s_nop 1
	v_cndmask_b32_e32 v72, v161, v72, vcc
	v_cmp_lt_i32_e32 vcc, 40, v184
	s_nop 1
	v_cndmask_b32_e32 v73, v161, v73, vcc
	v_cmp_lt_i32_e32 vcc, 41, v184
	s_nop 1
	v_cndmask_b32_e32 v74, v161, v74, vcc
	v_cmp_lt_i32_e32 vcc, 42, v184
	s_nop 1
	v_cndmask_b32_e32 v75, v161, v75, vcc
	v_cmp_lt_i32_e32 vcc, 47, v184
	s_nop 1
	v_cndmask_b32_e32 v76, v161, v76, vcc
	v_cmp_lt_i32_e32 vcc, 48, v184
	s_nop 1
	v_cndmask_b32_e32 v77, v161, v77, vcc
	v_cmp_lt_i32_e32 vcc, 49, v184
	s_nop 1
	v_cndmask_b32_e32 v78, v161, v78, vcc
	v_cmp_lt_i32_e32 vcc, 50, v184
	s_nop 1
	v_cndmask_b32_e32 v79, v161, v79, vcc
	v_cmp_lt_i32_e32 vcc, 55, v184
	s_nop 1
	v_cndmask_b32_e32 v80, v161, v80, vcc
	v_cmp_lt_i32_e32 vcc, 56, v184
	s_nop 1
	v_cndmask_b32_e32 v81, v161, v81, vcc
	v_cmp_lt_i32_e32 vcc, 57, v184
	s_nop 1
	v_cndmask_b32_e32 v82, v161, v82, vcc
	v_cmp_lt_i32_e32 vcc, 58, v184
	s_nop 1
	v_cndmask_b32_e32 v83, v161, v83, vcc

; template <int MODE> ...
;     ...
;         if (MODE == 1) { const unsigned mw = selw[bcur >> 5]; if (!((mw >> (bcur & 31)) & 1u)) nbl = -__builtin_inff(); }
; #pragma unroll
;         for (int r = 0; r < 16; ++r) { const float c0 = ks * (float)((r & 3) + 8 * (r >> 2)), c1 = c0 + 32.f * ks; p0[r] = fmaf(slope2, c0, p0[r]); p1[r] = fmaf(slope2, c1, p1[r]); }
;         if (bcur >= bA || bcur == bB) {
;             const float base = (float)dist0;
; #pragma unroll
;             for (int r = 0; r < 16; ++r) { const float c0 = ks * (float)((r & 3) + 8 * (r >> 2)), c1 = c0 + 32.f * ks; const float d0 = base - c0, d1 = base - c1;
;                 bool v0 = d0 >= 0.f, v1 = d1 >= 0.f;
;                 if (MODE == 2) { v0 = v0 && (d0 < 512.f); v1 = v1 && (d1 < 512.f); }
;                 p0[r] = v0 ? p0[r] : -__builtin_inff(); p1[r] = v1 ? p1[r] : -__builtin_inff(); }
.LBB0_780:
	v_lshl_add_u32 v188, s12, 6, v140
	s_ashr_i32 s13, s12, 5
	v_sub_u32_e32 v190, v166, v188
	v_lshl_add_u32 v188, s13, 2, v172
	ds_read_b32 v191, v188
	s_cmp_lt_i32 s12, s67
	s_cselect_b64 s[18:19], -1, 0
	s_cmp_lg_u32 s12, -1
	s_cselect_b64 s[20:21], -1, 0
	s_mov_b32 s84, s60
	s_mov_b32 s94, s65
	s_mov_b32 s74, s61
	s_and_b64 s[18:19], s[18:19], s[20:21]
	v_fma_f32 v189, 0, v134, v68
	v_add_f32_e32 v188, v134, v69
	v_fma_f32 v68, v134, s84, v84
	v_fma_f32 v69, v135, s85, v85
	v_fma_f32 v84, v134, s22, v70
	v_fma_f32 v85, v135, s23, v71
	v_fma_f32 v70, v134, s24, v86
	v_fma_f32 v71, v135, s25, v87
	v_fma_f32 v86, v134, s56, v72
	v_fma_f32 v87, v135, s57, v73
	v_fma_f32 v72, v134, s26, v88
	v_fma_f32 v73, v135, s27, v89
	v_fma_f32 v88, v134, s28, v74
	v_fma_f32 v89, v135, s29, v75
	v_fma_f32 v74, v134, s36, v90
	v_fma_f32 v75, v135, s37, v91
	v_fma_f32 v90, v134, s94, v76
	v_fma_f32 v91, v135, s95, v77
	v_fma_f32 v76, v134, s74, v92
	v_fma_f32 v77, v135, s75, v93
	v_fma_f32 v92, v134, s38, v78
	v_fma_f32 v93, v135, s39, v79
	v_fma_f32 v78, v134, s40, v94
	v_fma_f32 v79, v135, s41, v95
	v_fma_f32 v94, v134, s42, v80
	v_fma_f32 v95, v135, s43, v81
	v_fma_f32 v80, v134, s44, v96
	v_fma_f32 v81, v135, s45, v97
	v_fma_f32 v96, v134, s46, v82
	v_fma_f32 v97, v135, s47, v83
	v_fma_f32 v82, v134, s48, v98
	v_fma_f32 v83, v135, s49, v99
	s_and_b64 vcc, exec, s[18:19]
	s_cbranch_vccnz .LBB0_782
	v_cmp_lt_i32_e32 vcc, -1, v190
	s_nop 1
	v_cndmask_b32_e32 v189, v161, v189, vcc
	v_cmp_lt_i32_e32 vcc, 0, v190
	s_nop 1
	v_cndmask_b32_e32 v188, v161, v188, vcc
	v_cmp_lt_i32_e32 vcc, 1, v190
	s_nop 1
	v_cndmask_b32_e32 v84, v161, v84, vcc
	v_cmp_lt_i32_e32 vcc, 2, v190
	s_nop 1
	v_cndmask_b32_e32 v85, v161, v85, vcc
	v_cmp_lt_i32_e32 vcc, 7, v190
	s_nop 1
	v_cndmask_b32_e32 v86, v161, v86, vcc
	v_cmp_lt_i32_e32 vcc, 8, v190
	s_nop 1
	v_cndmask_b32_e32 v87, v161, v87, vcc
	v_cmp_lt_i32_e32 vcc, 9, v190
	s_nop 1
	v_cndmask_b32_e32 v88, v161, v88, vcc
	v_cmp_lt_i32_e32 vcc, 10, v190
	s_nop 1
	v_cndmask_b32_e32 v89, v161, v89, vcc
	v_cmp_lt_i32_e32 vcc, 15, v190
	s_nop 1
	v_cndmask_b32_e32 v90, v161, v90, vcc
	v_cmp_lt_i32_e32 vcc, 16, v190
	s_nop 1
	v_cndmask_b32_e32 v91, v161, v91, vcc
	v_cmp_lt_i32_e32 vcc, 17, v190
	s_nop 1
	v_cndmask_b32_e32 v92, v161, v92, vcc
	v_cmp_lt_i32_e32 vcc, 18, v190
	s_nop 1
	v_cndmask_b32_e32 v93, v161, v93, vcc
	v_cmp_lt_i32_e32 vcc, 23, v190
	s_nop 1
	v_cndmask_b32_e32 v94, v161, v94, vcc
	v_cmp_lt_i32_e32 vcc, 24, v190
	s_nop 1
	v_cndmask_b32_e32 v95, v161, v95, vcc
	v_cmp_lt_i32_e32 vcc, 25, v190
	s_nop 1
	v_cndmask_b32_e32 v96, v161, v96, vcc
	v_cmp_lt_i32_e32 vcc, 26, v190
	s_nop 1
	v_cndmask_b32_e32 v97, v161, v97, vcc
	v_cmp_lt_i32_e32 vcc, 31, v190
	s_nop 1
	v_cndmask_b32_e32 v68, v161, v68, vcc
	v_cmp_lt_i32_e32 vcc, 32, v190
	s_nop 1
	v_cndmask_b32_e32 v69, v161, v69, vcc
	v_cmp_lt_i32_e32 vcc, 33, v190
	s_nop 1
	v_cndmask_b32_e32 v70, v161, v70, vcc
	v_cmp_lt_i32_e32 vcc, 34, v190
	s_nop 1
	v_cndmask_b32_e32 v71, v161, v71, vcc
	v_cmp_lt_i32_e32 vcc, 39, v190
	s_nop 1
	v_cndmask_b32_e32 v72, v161, v72, vcc
	v_cmp_lt_i32_e32 vcc, 40, v190
	s_nop 1
	v_cndmask_b32_e32 v73, v161, v73, vcc
	v_cmp_lt_i32_e32 vcc, 41, v190
	s_nop 1
	v_cndmask_b32_e32 v74, v161, v74, vcc
	v_cmp_lt_i32_e32 vcc, 42, v190
	s_nop 1
	v_cndmask_b32_e32 v75, v161, v75, vcc
	v_cmp_lt_i32_e32 vcc, 47, v190
	s_nop 1
	v_cndmask_b32_e32 v76, v161, v76, vcc
	v_cmp_lt_i32_e32 vcc, 48, v190
	s_nop 1
	v_cndmask_b32_e32 v77, v161, v77, vcc
	v_cmp_lt_i32_e32 vcc, 49, v190
	s_nop 1
	v_cndmask_b32_e32 v78, v161, v78, vcc
	v_cmp_lt_i32_e32 vcc, 50, v190
	s_nop 1
	v_cndmask_b32_e32 v79, v161, v79, vcc
	v_cmp_lt_i32_e32 vcc, 55, v190
	s_nop 1
	v_cndmask_b32_e32 v80, v161, v80, vcc
	v_cmp_lt_i32_e32 vcc, 56, v190
	s_nop 1
	v_cndmask_b32_e32 v81, v161, v81, vcc
	v_cmp_lt_i32_e32 vcc, 57, v190
	s_nop 1
	v_cndmask_b32_e32 v82, v161, v82, vcc
	v_cmp_lt_i32_e32 vcc, 58, v190
	s_nop 1
	v_cndmask_b32_e32 v83, v161, v83, vcc

; template <int MODE> ...
;     ...
;         const int dist0 = (MODE == 0) ? (t - 31 - 1024 * bcur - 64 * hi) : (t - 64 * bcur - 4 * hi);
;         float nbl = -slope2 * (float)dist0;
;         if (MODE == 1) { const unsigned mw = selw[bcur >> 5]; if (!((mw >> (bcur & 31)) & 1u)) nbl = -__builtin_inff(); }
; #pragma unroll
;         for (int r = 0; r < 16; ++r) { const float c0 = ks * (float)((r & 3) + 8 * (r >> 2)), c1 = c0 + 32.f * ks; p0[r] = fmaf(slope2, c0, p0[r]); p1[r] = fmaf(slope2, c1, p1[r]); }
;         if (bcur >= bA || bcur == bB) {
;             const float base = (float)dist0;
; #pragma unroll
;             for (int r = 0; r < 16; ++r) { const float c0 = ks * (float)((r & 3) + 8 * (r >> 2)), c1 = c0 + 32.f * ks; const float d0 = base - c0, d1 = base - c1;
;                 bool v0 = d0 >= 0.f, v1 = d1 >= 0.f;
;                 if (MODE == 2) { v0 = v0 && (d0 < 512.f); v1 = v1 && (d1 < 512.f); }
;                 p0[r] = v0 ? p0[r] : -__builtin_inff(); p1[r] = v1 ? p1[r] : -__builtin_inff(); }
.LBB0_804:
	s_nop 7
	v_mov_b32_e32 v4, v9
	v_mov_b32_e32 v5, v10
	s_mov_b32 s10, s23
	s_mov_b32 s11, s56
	v_fma_f32 v38, v134, s10, v4
	v_fma_f32 v39, v134, s11, v5
	v_mov_b32_e32 v4, v11
	v_mov_b32_e32 v5, v12
	s_mov_b32 s10, s57
	s_mov_b32 s11, s28
	v_fma_f32 v42, v134, s10, v4
	v_fma_f32 v43, v134, s11, v5
	v_mov_b32_e32 v4, v13
	v_mov_b32_e32 v5, v14
	s_mov_b32 s10, s29
	s_mov_b32 s11, s13
	v_fma_f32 v44, v134, s10, v4
	v_fma_f32 v45, v134, s11, v5
	v_mov_b32_e32 v4, v15
	v_mov_b32_e32 v5, v16
	s_mov_b32 s10, s95
	s_mov_b32 s11, s38
	s_add_i32 s7, s67, -8
	v_lshl_add_u32 v2, s8, 6, v140
	v_fma_f32 v46, v134, s10, v4
	v_fma_f32 v47, v134, s11, v5
	v_mov_b32_e32 v4, v17
	v_mov_b32_e32 v5, v18
	s_mov_b32 s10, s39
	s_mov_b32 s11, s42
	v_sub_u32_e32 v2, v166, v2
	v_fma_f32 v48, v134, s10, v4
	v_fma_f32 v49, v134, s11, v5
	v_mov_b32_e32 v4, v19
	v_mov_b32_e32 v5, v20
	s_mov_b32 s10, s43
	s_mov_b32 s11, s46
	s_cmp_lt_i32 s8, s67
	v_cvt_f32_i32_e32 v40, v2
	v_fma_f32 v50, v134, s10, v4
	v_fma_f32 v51, v134, s11, v5
	s_cselect_b64 s[10:11], -1, 0
	s_cmp_lg_u32 s8, s7
	s_barrier
	s_cselect_b64 s[8:9], -1, 0
	s_mov_b32 s84, s60
	s_mov_b32 s74, s61
	s_and_b64 s[8:9], s[10:11], s[8:9]
	v_fma_f32 v52, 0, v134, v6
	v_add_f32_e32 v41, v134, v7
	v_fma_f32 v22, v134, s84, v22
	v_fma_f32 v23, v134, s85, v23
	v_fma_f32 v53, 2.0, v134, v8
	v_fma_f32 v24, v134, s24, v24
	v_fma_f32 v25, v134, s25, v25
	v_fma_f32 v26, v134, s26, v26
	v_fma_f32 v27, v134, s27, v27
	v_fma_f32 v28, v134, s36, v28
	v_fma_f32 v29, v134, s37, v29
	v_fma_f32 v30, v134, s74, v30
	v_fma_f32 v31, v134, s75, v31
	v_fma_f32 v32, v134, s40, v32
	v_fma_f32 v33, v134, s41, v33
	v_fma_f32 v34, v134, s44, v34
	v_fma_f32 v35, v134, s45, v35
	v_fmac_f32_e32 v21, 0x41d80000, v134
	v_fma_f32 v36, v134, s48, v36
	v_fma_f32 v37, v134, s49, v37
	s_and_b64 vcc, exec, s[8:9]
	s_cbranch_vccnz .LBB0_806
; template <int MODE> ...
;     ...
;             for (int r = 0; r < 16; ++r) { const float c0 = ks * (float)((r & 3) + 8 * (r >> 2)), c1 = c0 + 32.f * ks; const float d0 = base - c0, d1 = base - c1;
;                 bool v0 = d0 >= 0.f, v1 = d1 >= 0.f;
;                 if (MODE == 2) { v0 = v0 && (d0 < 512.f); v1 = v1 && (d1 < 512.f); }
;                 p0[r] = v0 ? p0[r] : -__builtin_inff(); p1[r] = v1 ? p1[r] : -__builtin_inff(); }
	s_mov_b32 s8, 0xc2000000
	s_mov_b32 s9, 0xc2040000
	v_add_f32_e32 v4, s8, v40
	v_add_f32_e32 v5, s9, v40
	s_movk_i32 s8, 0x200
	v_cmp_gt_u32_e32 vcc, s8, v2
	s_mov_b32 s8, -1.0
	s_mov_b32 s9, -2.0
	v_add_f32_e32 v6, s8, v40
	v_add_f32_e32 v7, s9, v40
	s_mov_b32 s8, 0xc2080000
	v_cndmask_b32_e32 v52, v161, v52, vcc
	s_mov_b32 s9, 0xc20c0000
	v_cmp_le_f32_e32 vcc, 0, v6
	v_cmp_gt_f32_e64 s[10:11], s82, v6
	v_add_f32_e32 v8, s8, v40
	v_add_f32_e32 v9, s9, v40
	v_cmp_le_f32_e64 s[8:9], 0, v7
	v_cmp_gt_f32_e64 s[12:13], s82, v7
	s_and_b64 vcc, vcc, s[10:11]
	v_cndmask_b32_e32 v41, v161, v41, vcc
	s_and_b64 vcc, s[8:9], s[12:13]
	s_mov_b32 s8, 0xc0400000
	s_mov_b32 s9, 0xc1000000
	v_add_f32_e32 v6, s8, v40
	v_add_f32_e32 v7, s9, v40
	s_mov_b32 s8, 0xc2200000
	v_cndmask_b32_e32 v53, v161, v53, vcc
	s_mov_b32 s9, 0xc2240000
	v_cmp_le_f32_e32 vcc, 0, v6
	v_cmp_gt_f32_e64 s[10:11], s82, v6
	v_add_f32_e32 v10, s8, v40
	v_add_f32_e32 v11, s9, v40
	v_cmp_le_f32_e64 s[8:9], 0, v7
	v_cmp_gt_f32_e64 s[12:13], s82, v7
	s_and_b64 vcc, vcc, s[10:11]
	v_cndmask_b32_e32 v38, v161, v38, vcc
	s_and_b64 vcc, s[8:9], s[12:13]
	s_mov_b32 s8, 0xc1100000
	s_mov_b32 s9, 0xc1200000
	v_add_f32_e32 v6, s8, v40
	v_add_f32_e32 v7, s9, v40
	s_mov_b32 s8, 0xc2280000
	v_cndmask_b32_e32 v39, v161, v39, vcc
	s_mov_b32 s9, 0xc22c0000
	v_cmp_le_f32_e32 vcc, 0, v6
	v_cmp_gt_f32_e64 s[10:11], s82, v6
	v_add_f32_e32 v12, s8, v40
	v_add_f32_e32 v13, s9, v40
	v_cmp_le_f32_e64 s[8:9], 0, v7
	v_cmp_gt_f32_e64 s[12:13], s82, v7
	s_and_b64 vcc, vcc, s[10:11]
	v_cndmask_b32_e32 v42, v161, v42, vcc
	s_and_b64 vcc, s[8:9], s[12:13]
	s_mov_b32 s8, 0xc1300000
	s_mov_b32 s9, 0xc1800000
	v_add_f32_e32 v6, s8, v40
	v_add_f32_e32 v7, s9, v40
	s_mov_b32 s8, 0xc2400000
	v_cndmask_b32_e32 v43, v161, v43, vcc
	s_mov_b32 s9, 0xc2440000
	v_cmp_le_f32_e32 vcc, 0, v6
	v_cmp_gt_f32_e64 s[10:11], s82, v6
	v_add_f32_e32 v14, s8, v40
	v_add_f32_e32 v15, s9, v40
	v_cmp_le_f32_e64 s[8:9], 0, v7
	v_cmp_gt_f32_e64 s[12:13], s82, v7
	s_and_b64 vcc, vcc, s[10:11]
	v_cndmask_b32_e32 v44, v161, v44, vcc
	s_and_b64 vcc, s[8:9], s[12:13]
	s_mov_b32 s8, 0xc1880000
	s_mov_b32 s9, 0xc1900000
	v_add_f32_e32 v6, s8, v40
	v_add_f32_e32 v7, s9, v40
	s_mov_b32 s8, 0xc2480000
	v_cndmask_b32_e32 v45, v161, v45, vcc
	s_mov_b32 s9, 0xc24c0000
	v_cmp_le_f32_e32 vcc, 0, v6
	v_cmp_gt_f32_e64 s[10:11], s82, v6
	v_add_f32_e32 v16, s8, v40
	v_add_f32_e32 v17, s9, v40
	v_cmp_le_f32_e64 s[8:9], 0, v7
	v_cmp_gt_f32_e64 s[12:13], s82, v7
	s_and_b64 vcc, vcc, s[10:11]
	v_cndmask_b32_e32 v46, v161, v46, vcc
	s_and_b64 vcc, s[8:9], s[12:13]
	s_mov_b32 s8, 0xc1980000
	s_mov_b32 s9, 0xc1c00000
	v_add_f32_e32 v6, s8, v40
	v_add_f32_e32 v7, s9, v40
	s_mov_b32 s8, 0xc2600000
	v_cndmask_b32_e32 v47, v161, v47, vcc
	s_mov_b32 s9, 0xc2640000
	v_cmp_le_f32_e32 vcc, 0, v6
	v_cmp_gt_f32_e64 s[10:11], s82, v6
	v_add_f32_e32 v18, s8, v40
	v_add_f32_e32 v19, s9, v40
	v_cmp_le_f32_e64 s[8:9], 0, v7
	v_cmp_gt_f32_e64 s[12:13], s82, v7
	s_and_b64 vcc, vcc, s[10:11]
	v_cndmask_b32_e32 v48, v161, v48, vcc
	s_and_b64 vcc, s[8:9], s[12:13]
	s_mov_b32 s8, 0xc1c80000
	s_mov_b32 s9, 0xc1d00000
	v_add_f32_e32 v6, s8, v40
	v_add_f32_e32 v7, s9, v40
	s_mov_b32 s8, 0xc2680000
	v_cndmask_b32_e32 v49, v161, v49, vcc
	s_mov_b32 s9, 0xc26c0000
	v_cmp_le_f32_e32 vcc, 0, v6
	v_cmp_gt_f32_e64 s[10:11], s82, v6
	v_add_f32_e32 v54, s8, v40
	v_add_f32_e32 v55, s9, v40
	v_cmp_le_f32_e64 s[8:9], 0, v7
	v_cmp_gt_f32_e64 s[12:13], s82, v7
	s_and_b64 vcc, vcc, s[10:11]
	v_cmp_le_f32_e64 s[10:11], 0, v8
	v_cmp_gt_f32_e64 s[44:45], s82, v8
	v_cndmask_b32_e32 v50, v161, v50, vcc
	s_and_b64 vcc, s[8:9], s[12:13]
	v_add_f32_e32 v2, 0xc1d80000, v40
	v_cmp_le_f32_e64 s[12:13], 0, v9
	v_cmp_gt_f32_e64 s[46:47], s82, v9
	s_and_b64 s[10:11], s[10:11], s[44:45]
	v_cndmask_b32_e32 v51, v161, v51, vcc
	v_cmp_le_f32_e32 vcc, 0, v2
	v_cmp_gt_f32_e64 s[8:9], s82, v2
	v_cmp_le_f32_e64 s[14:15], 0, v10
	v_cmp_gt_f32_e64 s[48:49], s82, v10
	v_cndmask_b32_e64 v24, v161, v24, s[10:11]
	s_and_b64 s[10:11], s[12:13], s[46:47]
	s_and_b64 vcc, vcc, s[8:9]
	s_mov_b32 s74, s17
	v_cmp_le_f32_e64 s[16:17], 0, v11
	v_cmp_gt_f32_e64 s[50:51], s82, v11
	v_cndmask_b32_e64 v25, v161, v25, s[10:11]
	s_and_b64 s[10:11], s[14:15], s[48:49]
	v_cndmask_b32_e32 v21, v161, v21, vcc
	v_cmp_le_f32_e32 vcc, 0, v4
	v_cmp_le_f32_e64 s[18:19], 0, v12
	v_cmp_gt_f32_e64 s[40:41], s82, v4
	v_cmp_gt_f32_e64 s[52:53], s82, v12
	v_cndmask_b32_e64 v26, v161, v26, s[10:11]
	s_and_b64 s[10:11], s[16:17], s[50:51]
	v_cmp_le_f32_e64 s[20:21], 0, v13
	v_cmp_gt_f32_e64 s[54:55], s82, v13
	s_and_b64 vcc, vcc, s[40:41]
	v_cndmask_b32_e64 v27, v161, v27, s[10:11]
	s_and_b64 s[10:11], s[18:19], s[52:53]
	v_cmp_le_f32_e64 s[8:9], 0, v5
	v_cmp_le_f32_e64 s[22:23], 0, v14
	v_cmp_le_f32_e64 s[30:31], 0, v18
	v_cmp_gt_f32_e64 s[42:43], s82, v5
	v_cmp_gt_f32_e64 s[56:57], s82, v14
	v_cndmask_b32_e32 v22, v161, v22, vcc
	v_cmp_gt_f32_e32 vcc, s82, v18
	v_cndmask_b32_e64 v28, v161, v28, s[10:11]
	s_and_b64 s[10:11], s[20:21], s[54:55]
	v_cmp_le_f32_e64 s[24:25], 0, v15
	v_cmp_le_f32_e64 s[34:35], 0, v19
	v_cmp_gt_f32_e64 s[58:59], s82, v15
	s_and_b64 s[8:9], s[8:9], s[42:43]
	v_cmp_gt_f32_e64 s[42:43], s82, v19
	v_cndmask_b32_e64 v29, v161, v29, s[10:11]
	s_and_b64 s[10:11], s[22:23], s[56:57]
	s_and_b64 vcc, s[30:31], vcc
	v_cmp_le_f32_e64 s[26:27], 0, v16
	v_cmp_le_f32_e64 s[36:37], 0, v54
	v_cmp_gt_f32_e64 s[60:61], s82, v16
	v_cndmask_b32_e64 v23, v161, v23, s[8:9]
	v_cmp_gt_f32_e64 s[8:9], s82, v54
	v_cndmask_b32_e64 v30, v161, v30, s[10:11]
	s_and_b64 s[10:11], s[24:25], s[58:59]
	v_cndmask_b32_e32 v34, v161, v34, vcc
	s_and_b64 vcc, s[34:35], s[42:43]
	v_cmp_le_f32_e64 s[28:29], 0, v17
	v_cmp_le_f32_e64 s[38:39], 0, v55
	v_cmp_gt_f32_e64 s[40:41], s82, v17
	v_cmp_gt_f32_e64 s[44:45], s82, v55
	v_cndmask_b32_e64 v31, v161, v31, s[10:11]
	s_and_b64 s[10:11], s[26:27], s[60:61]
	v_cndmask_b32_e32 v35, v161, v35, vcc
	s_and_b64 vcc, s[36:37], s[8:9]
	s_mov_b32 s48, 0x42680000
	v_readlane_b32 s50, v245, 61
	s_mov_b32 s56, 0x41000000
	s_mov_b32 s58, 0x44480000
	s_mov_b32 s60, 0x42000000
	v_cndmask_b32_e64 v32, v161, v32, s[10:11]
	s_and_b64 s[10:11], s[28:29], s[40:41]
	s_mov_b32 s40, 0x42480000
	s_mov_b32 s42, 0x41c00000
	v_cndmask_b32_e32 v36, v161, v36, vcc
	s_and_b64 vcc, s[38:39], s[44:45]
	s_mov_b32 s44, 0x42600000
	s_mov_b32 s38, 0x41900000
	s_mov_b32 s36, 0x42280000
	s_mov_b32 s28, 0x41200000
	s_mov_b32 s26, 0x42200000
	s_mov_b32 s24, 0x42080000
	s_mov_b32 s22, 2.0
	s_mov_b32 s46, 0x41d00000
	s_mov_b32 s49, 0x426c0000
	s_mov_b32 s17, s74
	v_readlane_b32 s51, v245, 62
	s_mov_b32 s57, 0x41100000
	s_mov_b32 s59, 0x444c0000
	s_mov_b32 s61, 0x42400000
	s_mov_b32 s41, 0x424c0000
	v_cndmask_b32_e64 v33, v161, v33, s[10:11]
	v_readlane_b32 s31, v245, 58
	s_mov_b32 s43, 0x41c80000
	s_mov_b32 s45, 0x42640000
	s_mov_b32 s39, 0x41980000
	s_mov_b32 s37, 0x422c0000
	s_mov_b32 s29, 0x41300000
	s_mov_b32 s27, 0x42240000
	s_mov_b32 s25, 0x420c0000
	s_mov_b32 s23, 0x40400000
	v_cndmask_b32_e32 v37, v161, v37, vcc
	s_mov_b32 s47, 0x41d80000

; template <int MODE> ...
;     ...
;         const int dist0 = (MODE == 0) ? (t - 31 - 1024 * bcur - 64 * hi) : (t - 64 * bcur - 4 * hi);
;         float nbl = -slope2 * (float)dist0;
;         if (MODE == 1) { const unsigned mw = selw[bcur >> 5]; if (!((mw >> (bcur & 31)) & 1u)) nbl = -__builtin_inff(); }
; #pragma unroll
;         for (int r = 0; r < 16; ++r) { const float c0 = ks * (float)((r & 3) + 8 * (r >> 2)), c1 = c0 + 32.f * ks; p0[r] = fmaf(slope2, c0, p0[r]); p1[r] = fmaf(slope2, c1, p1[r]); }
;         if (bcur >= bA || bcur == bB) {
;             const float base = (float)dist0;
; #pragma unroll
;             for (int r = 0; r < 16; ++r) { const float c0 = ks * (float)((r & 3) + 8 * (r >> 2)), c1 = c0 + 32.f * ks; const float d0 = base - c0, d1 = base - c1;
;                 bool v0 = d0 >= 0.f, v1 = d1 >= 0.f;
;                 if (MODE == 2) { v0 = v0 && (d0 < 512.f); v1 = v1 && (d1 < 512.f); }
;                 p0[r] = v0 ? p0[r] : -__builtin_inff(); p1[r] = v1 ? p1[r] : -__builtin_inff(); }
.LBB0_818:
	s_mov_b32 s84, s60
	v_fma_f32 v187, 2.0, v134, v70
	v_mov_b32_e32 v70, v71
	v_mov_b32_e32 v71, v72
	s_mov_b32 s14, s23
	s_mov_b32 s15, s56
	v_fma_f32 v188, 0, v134, v68
	v_add_f32_e32 v186, v134, v69
	v_fma_f32 v68, v134, s84, v84
	v_fma_f32 v69, v135, s85, v85
	v_fma_f32 v84, v134, s24, v86
	v_fma_f32 v85, v135, s25, v87
	v_fma_f32 v86, v134, s14, v70
	v_fma_f32 v87, v135, s15, v71
	v_mov_b32_e32 v72, v73
	v_mov_b32_e32 v73, v74
	s_mov_b32 s14, s57
	s_mov_b32 s15, s28
	v_fma_f32 v70, v134, s26, v88
	v_fma_f32 v71, v135, s27, v89
	v_fma_f32 v88, v134, s14, v72
	v_fma_f32 v89, v135, s15, v73
	v_mov_b32_e32 v74, v75
	v_mov_b32_e32 v75, v76
	s_mov_b32 s14, s29
	s_mov_b32 s15, s65
	v_fma_f32 v72, v134, s36, v90
	v_fma_f32 v73, v135, s37, v91
	v_fma_f32 v90, v134, s14, v74
	v_fma_f32 v91, v135, s15, v75
	s_mov_b32 s74, s61
	v_mov_b32_e32 v76, v77
	v_mov_b32_e32 v77, v78
	s_mov_b32 s14, s95
	s_mov_b32 s15, s38
	v_lshl_add_u32 v2, s12, 6, v140
	v_fma_f32 v74, v134, s74, v92
	v_fma_f32 v75, v135, s75, v93
	v_fma_f32 v92, v134, s14, v76
	v_fma_f32 v93, v135, s15, v77
	v_mov_b32_e32 v78, v79
	v_mov_b32_e32 v79, v80
	s_mov_b32 s14, s39
	s_mov_b32 s15, s42
	v_sub_u32_e32 v184, v166, v2
	v_fma_f32 v76, v134, s40, v94
	v_fma_f32 v77, v135, s41, v95
	v_fma_f32 v94, v134, s14, v78
	v_fma_f32 v95, v135, s15, v79
	v_mov_b32_e32 v80, v81
	v_mov_b32_e32 v81, v82
	s_mov_b32 s14, s43
	s_mov_b32 s15, s46
	s_cmp_lt_i32 s12, s67
	v_cvt_f32_i32_e32 v2, v184
	v_fma_f32 v78, v134, s44, v96
	v_fma_f32 v79, v135, s45, v97
	v_fma_f32 v96, v134, s14, v80
	v_fma_f32 v97, v135, s15, v81
	s_cselect_b64 s[14:15], -1, 0
	s_cmp_lg_u32 s12, s7
	s_cselect_b64 s[12:13], -1, 0
	s_and_b64 s[12:13], s[14:15], s[12:13]
	v_fmac_f32_e32 v83, 0x41d80000, v134
	v_fma_f32 v80, v134, s48, v98
	v_fma_f32 v81, v135, s49, v99
	s_and_b64 vcc, exec, s[12:13]
	s_cbranch_vccnz .LBB0_820
	s_mov_b32 s12, 0xc2000000
	s_mov_b32 s13, 0xc2040000
	v_add_f32_e32 v98, s12, v2
	v_add_f32_e32 v99, s13, v2
	s_movk_i32 s12, 0x200
	v_cmp_gt_u32_e32 vcc, s12, v184
	s_mov_b32 s12, -1.0
	s_mov_b32 s13, -2.0
	v_add_f32_e32 v190, s12, v2
	v_add_f32_e32 v191, s13, v2
	s_mov_b32 s12, 0xc2080000
	v_cndmask_b32_e32 v188, v161, v188, vcc
	s_mov_b32 s13, 0xc20c0000
	v_cmp_le_f32_e32 vcc, 0, v190
	v_cmp_gt_f32_e64 s[14:15], s82, v190
	v_add_f32_e32 v192, s12, v2
	v_add_f32_e32 v193, s13, v2
	v_cmp_le_f32_e64 s[12:13], 0, v191
	v_cmp_gt_f32_e64 s[16:17], s82, v191
	s_and_b64 vcc, vcc, s[14:15]
	v_cndmask_b32_e32 v186, v161, v186, vcc
	s_and_b64 vcc, s[12:13], s[16:17]
	s_mov_b32 s12, 0xc0400000
	s_mov_b32 s13, 0xc1000000
	v_add_f32_e32 v190, s12, v2
	v_add_f32_e32 v191, s13, v2
	s_mov_b32 s12, 0xc2200000
	v_cndmask_b32_e32 v187, v161, v187, vcc
	s_mov_b32 s13, 0xc2240000
	v_cmp_le_f32_e32 vcc, 0, v190
	v_cmp_gt_f32_e64 s[14:15], s82, v190
	v_add_f32_e32 v196, s12, v2
	v_add_f32_e32 v197, s13, v2
	v_cmp_le_f32_e64 s[12:13], 0, v191
	v_cmp_gt_f32_e64 s[16:17], s82, v191
	s_and_b64 vcc, vcc, s[14:15]
	v_cndmask_b32_e32 v86, v161, v86, vcc
	s_and_b64 vcc, s[12:13], s[16:17]
	s_mov_b32 s12, 0xc1100000
	s_mov_b32 s13, 0xc1200000
	v_add_f32_e32 v190, s12, v2
	v_add_f32_e32 v191, s13, v2
	s_mov_b32 s12, 0xc2280000
	v_cndmask_b32_e32 v87, v161, v87, vcc
	s_mov_b32 s13, 0xc22c0000
	v_cmp_le_f32_e32 vcc, 0, v190
	v_cmp_gt_f32_e64 s[14:15], s82, v190
	v_add_f32_e32 v198, s12, v2
	v_add_f32_e32 v199, s13, v2
	v_cmp_le_f32_e64 s[12:13], 0, v191
	v_cmp_gt_f32_e64 s[16:17], s82, v191
	s_and_b64 vcc, vcc, s[14:15]
	v_cndmask_b32_e32 v88, v161, v88, vcc
	s_and_b64 vcc, s[12:13], s[16:17]
	s_mov_b32 s12, 0xc1300000
	s_mov_b32 s13, 0xc1800000
	v_add_f32_e32 v190, s12, v2
	v_add_f32_e32 v191, s13, v2
	s_mov_b32 s12, 0xc2400000
	v_cndmask_b32_e32 v89, v161, v89, vcc
	s_mov_b32 s13, 0xc2440000
	v_cmp_le_f32_e32 vcc, 0, v190
	v_cmp_gt_f32_e64 s[14:15], s82, v190
	v_add_f32_e32 v200, s12, v2
	v_add_f32_e32 v201, s13, v2
	v_cmp_le_f32_e64 s[12:13], 0, v191
	v_cmp_gt_f32_e64 s[16:17], s82, v191
	s_and_b64 vcc, vcc, s[14:15]
	v_cndmask_b32_e32 v90, v161, v90, vcc
	s_and_b64 vcc, s[12:13], s[16:17]
	s_mov_b32 s12, 0xc1880000
	s_mov_b32 s13, 0xc1900000
	v_add_f32_e32 v190, s12, v2
	v_add_f32_e32 v191, s13, v2
	s_mov_b32 s12, 0xc2480000
	v_cndmask_b32_e32 v91, v161, v91, vcc
	s_mov_b32 s13, 0xc24c0000
	v_cmp_le_f32_e32 vcc, 0, v190
	v_cmp_gt_f32_e64 s[14:15], s82, v190
	v_add_f32_e32 v202, s12, v2
	v_add_f32_e32 v203, s13, v2
	v_cmp_le_f32_e64 s[12:13], 0, v191
	v_cmp_gt_f32_e64 s[16:17], s82, v191
	s_and_b64 vcc, vcc, s[14:15]
	v_cndmask_b32_e32 v92, v161, v92, vcc
	s_and_b64 vcc, s[12:13], s[16:17]
; template <int MODE> ...
;     ...
;             for (int r = 0; r < 16; ++r) { const float c0 = ks * (float)((r & 3) + 8 * (r >> 2)), c1 = c0 + 32.f * ks; const float d0 = base - c0, d1 = base - c1;
;                 bool v0 = d0 >= 0.f, v1 = d1 >= 0.f;
;                 if (MODE == 2) { v0 = v0 && (d0 < 512.f); v1 = v1 && (d1 < 512.f); }
;                 p0[r] = v0 ? p0[r] : -__builtin_inff(); p1[r] = v1 ? p1[r] : -__builtin_inff(); }
	s_mov_b32 s12, 0xc1980000
	s_mov_b32 s13, 0xc1c00000
	v_add_f32_e32 v190, s12, v2
	v_add_f32_e32 v191, s13, v2
	s_mov_b32 s12, 0xc2600000
	v_cndmask_b32_e32 v93, v161, v93, vcc
	s_mov_b32 s13, 0xc2640000
	v_cmp_le_f32_e32 vcc, 0, v190
	v_cmp_gt_f32_e64 s[14:15], s82, v190
	v_add_f32_e32 v204, s12, v2
	v_add_f32_e32 v205, s13, v2
	v_cmp_le_f32_e64 s[12:13], 0, v191
	v_cmp_gt_f32_e64 s[16:17], s82, v191
	s_and_b64 vcc, vcc, s[14:15]
	v_cndmask_b32_e32 v94, v161, v94, vcc
	s_and_b64 vcc, s[12:13], s[16:17]
	s_mov_b32 s12, 0xc1c80000
	s_mov_b32 s13, 0xc1d00000
	v_add_f32_e32 v190, s12, v2
	v_add_f32_e32 v191, s13, v2
	s_mov_b32 s12, 0xc2680000
	v_cndmask_b32_e32 v95, v161, v95, vcc
	s_mov_b32 s13, 0xc26c0000
	v_cmp_le_f32_e32 vcc, 0, v190
	v_cmp_gt_f32_e64 s[14:15], s82, v190
	v_add_f32_e32 v206, s12, v2
	v_add_f32_e32 v207, s13, v2
	v_cmp_le_f32_e64 s[12:13], 0, v191
	v_cmp_gt_f32_e64 s[16:17], s82, v191
	s_and_b64 vcc, vcc, s[14:15]
	v_cmp_le_f32_e64 s[14:15], 0, v192
	v_cmp_gt_f32_e64 s[48:49], s82, v192
	v_cndmask_b32_e32 v96, v161, v96, vcc
	s_and_b64 vcc, s[12:13], s[16:17]
	v_add_f32_e32 v82, 0xc1d80000, v2
	v_cmp_le_f32_e64 s[16:17], 0, v193
	v_cmp_gt_f32_e64 s[50:51], s82, v193
	s_and_b64 s[14:15], s[14:15], s[48:49]
	v_cndmask_b32_e32 v97, v161, v97, vcc
	v_cmp_le_f32_e32 vcc, 0, v82
	v_cmp_gt_f32_e64 s[12:13], s82, v82
	v_cmp_le_f32_e64 s[18:19], 0, v196
	v_cmp_gt_f32_e64 s[52:53], s82, v196
	v_cndmask_b32_e64 v84, v161, v84, s[14:15]
	s_and_b64 s[14:15], s[16:17], s[50:51]
	s_and_b64 vcc, vcc, s[12:13]
	v_cmp_le_f32_e64 s[20:21], 0, v197
	v_cmp_gt_f32_e64 s[54:55], s82, v197
	v_cndmask_b32_e64 v85, v161, v85, s[14:15]
	s_and_b64 s[14:15], s[18:19], s[52:53]
	v_cndmask_b32_e32 v83, v161, v83, vcc
	v_cmp_le_f32_e32 vcc, 0, v98
	v_cmp_le_f32_e64 s[22:23], 0, v198
	v_cmp_gt_f32_e64 s[44:45], s82, v98
	v_cmp_gt_f32_e64 s[56:57], s82, v198
	v_cndmask_b32_e64 v70, v161, v70, s[14:15]
	s_and_b64 s[14:15], s[20:21], s[54:55]
	v_cmp_le_f32_e64 s[24:25], 0, v199
	v_cmp_gt_f32_e64 s[58:59], s82, v199
	s_and_b64 vcc, vcc, s[44:45]
	v_cndmask_b32_e64 v71, v161, v71, s[14:15]
	s_and_b64 s[14:15], s[22:23], s[56:57]
	v_cmp_le_f32_e64 s[12:13], 0, v99
	v_cmp_le_f32_e64 s[26:27], 0, v200
	v_cmp_le_f32_e64 s[36:37], 0, v204
	v_cmp_gt_f32_e64 s[46:47], s82, v99
	v_cmp_gt_f32_e64 s[60:61], s82, v200
	v_cndmask_b32_e32 v68, v161, v68, vcc
	v_cmp_gt_f32_e32 vcc, s82, v204
	v_cndmask_b32_e64 v72, v161, v72, s[14:15]
	s_and_b64 s[14:15], s[24:25], s[58:59]
	v_cmp_le_f32_e64 s[28:29], 0, v201
	v_cmp_le_f32_e64 s[38:39], 0, v205
	v_cmp_gt_f32_e64 s[62:63], s82, v201
	s_and_b64 s[12:13], s[12:13], s[46:47]
	v_cmp_gt_f32_e64 s[46:47], s82, v205
	v_cndmask_b32_e64 v73, v161, v73, s[14:15]
	s_and_b64 s[14:15], s[26:27], s[60:61]
	s_and_b64 vcc, s[36:37], vcc
	v_cmp_le_f32_e64 s[30:31], 0, v202
	v_cmp_le_f32_e64 s[40:41], 0, v206
	v_cmp_gt_f32_e64 s[64:65], s82, v202
	v_cndmask_b32_e64 v69, v161, v69, s[12:13]
	v_cmp_gt_f32_e64 s[12:13], s82, v206
	v_cndmask_b32_e64 v74, v161, v74, s[14:15]
	s_and_b64 s[14:15], s[28:29], s[62:63]
	v_cndmask_b32_e32 v78, v161, v78, vcc
	s_and_b64 vcc, s[38:39], s[46:47]
	v_cmp_le_f32_e64 s[34:35], 0, v203
	v_cmp_le_f32_e64 s[42:43], 0, v207
	v_cmp_gt_f32_e64 s[44:45], s82, v203
	v_cmp_gt_f32_e64 s[48:49], s82, v207
	v_cndmask_b32_e64 v75, v161, v75, s[14:15]
	s_and_b64 s[14:15], s[30:31], s[64:65]
	v_cndmask_b32_e32 v79, v161, v79, vcc
	s_and_b64 vcc, s[40:41], s[12:13]
	v_readlane_b32 s50, v245, 61
	s_mov_b32 s56, 0x41000000
	s_mov_b32 s58, 0x44480000
	s_mov_b32 s60, 0x42000000
	s_mov_b32 s64, 0
	v_cndmask_b32_e64 v76, v161, v76, s[14:15]
	s_and_b64 s[14:15], s[34:35], s[44:45]
	s_mov_b32 s44, 0x42600000
	s_mov_b32 s38, 0x41900000
	s_mov_b32 s36, 0x42280000
	s_mov_b32 s28, 0x41200000
	s_mov_b32 s26, 0x42200000
	s_mov_b32 s24, 0x42080000
	s_mov_b32 s22, 2.0
	s_mov_b32 s40, 0x42480000
	v_cndmask_b32_e32 v80, v161, v80, vcc
	s_and_b64 vcc, s[42:43], s[48:49]
	s_mov_b32 s48, 0x42680000
	s_mov_b32 s42, 0x41c00000
	v_readlane_b32 s51, v245, 62
	s_mov_b32 s57, 0x41100000
	s_mov_b32 s59, 0x444c0000
	s_mov_b32 s61, 0x42400000
	v_readlane_b32 s31, v245, 58
	s_mov_b32 s65, 0x41800000
	s_mov_b32 s45, 0x42640000
	v_cndmask_b32_e64 v77, v161, v77, s[14:15]
	s_mov_b32 s46, 0x41d00000
	s_mov_b32 s39, 0x41980000
	s_mov_b32 s37, 0x422c0000
	s_mov_b32 s29, 0x41300000
	s_mov_b32 s27, 0x42240000
	s_mov_b32 s25, 0x420c0000
	s_mov_b32 s23, 0x40400000
	s_mov_b32 s41, 0x424c0000
	s_mov_b32 s49, 0x426c0000
	s_mov_b32 s43, 0x41c80000
	v_cndmask_b32_e32 v81, v161, v81, vcc
	s_mov_b32 s47, 0x41d80000

; template <int MODE> ...
;     ...
;         const int dist0 = (MODE == 0) ? (t - 31 - 1024 * bcur - 64 * hi) : (t - 64 * bcur - 4 * hi);
;         float nbl = -slope2 * (float)dist0;
;         if (MODE == 1) { const unsigned mw = selw[bcur >> 5]; if (!((mw >> (bcur & 31)) & 1u)) nbl = -__builtin_inff(); }
; #pragma unroll
;         for (int r = 0; r < 16; ++r) { const float c0 = ks * (float)((r & 3) + 8 * (r >> 2)), c1 = c0 + 32.f * ks; p0[r] = fmaf(slope2, c0, p0[r]); p1[r] = fmaf(slope2, c1, p1[r]); }
;         if (bcur >= bA || bcur == bB) {
;             const float base = (float)dist0;
; #pragma unroll
;             for (int r = 0; r < 16; ++r) { const float c0 = ks * (float)((r & 3) + 8 * (r >> 2)), c1 = c0 + 32.f * ks; const float d0 = base - c0, d1 = base - c1;
;                 bool v0 = d0 >= 0.f, v1 = d1 >= 0.f;
;                 if (MODE == 2) { v0 = v0 && (d0 < 512.f); v1 = v1 && (d1 < 512.f); }
;                 p0[r] = v0 ? p0[r] : -__builtin_inff(); p1[r] = v1 ? p1[r] : -__builtin_inff(); }
.LBB0_838:
	s_mov_b32 s84, s60
	s_nop 3
	v_fma_f32 v186, 2.0, v134, v70
	v_mov_b32_e32 v70, v71
	v_mov_b32_e32 v71, v72
	s_mov_b32 s14, s23
	s_mov_b32 s15, s56
	v_fma_f32 v187, 0, v134, v68
	v_add_f32_e32 v185, v134, v69
	v_fma_f32 v68, v134, s84, v84
	v_fma_f32 v69, v135, s85, v85
	v_fma_f32 v84, v134, s24, v86
	v_fma_f32 v85, v135, s25, v87
	v_fma_f32 v86, v134, s14, v70
	v_fma_f32 v87, v135, s15, v71
	v_mov_b32_e32 v72, v73
	v_mov_b32_e32 v73, v74
	s_mov_b32 s14, s57
	s_mov_b32 s15, s28
	v_fma_f32 v70, v134, s26, v88
	v_fma_f32 v71, v135, s27, v89
	v_fma_f32 v88, v134, s14, v72
	v_fma_f32 v89, v135, s15, v73
	v_mov_b32_e32 v74, v75
	v_mov_b32_e32 v75, v76
	s_mov_b32 s14, s29
	s_mov_b32 s15, s65
	v_fma_f32 v72, v134, s36, v90
	v_fma_f32 v73, v135, s37, v91
	v_fma_f32 v90, v134, s14, v74
	v_fma_f32 v91, v135, s15, v75
	s_mov_b32 s74, s61
	v_mov_b32_e32 v76, v77
	v_mov_b32_e32 v77, v78
	s_mov_b32 s14, s95
	s_mov_b32 s15, s38
	v_lshl_add_u32 v2, s12, 6, v140
	v_fma_f32 v74, v134, s74, v92
	v_fma_f32 v75, v135, s75, v93
	v_fma_f32 v92, v134, s14, v76
	v_fma_f32 v93, v135, s15, v77
	v_mov_b32_e32 v78, v79
	v_mov_b32_e32 v79, v80
	s_mov_b32 s14, s39
	s_mov_b32 s15, s42
	v_sub_u32_e32 v188, v166, v2
	v_fma_f32 v76, v134, s40, v94
	v_fma_f32 v77, v135, s41, v95
	v_fma_f32 v94, v134, s14, v78
	v_fma_f32 v95, v135, s15, v79
	v_mov_b32_e32 v80, v81
	v_mov_b32_e32 v81, v82
	s_mov_b32 s14, s43
	s_mov_b32 s15, s46
	s_cmp_lt_i32 s12, s67
	v_cvt_f32_i32_e32 v2, v188
	v_fma_f32 v78, v134, s44, v96
	v_fma_f32 v79, v135, s45, v97
	v_fma_f32 v96, v134, s14, v80
	v_fma_f32 v97, v135, s15, v81
	s_cselect_b64 s[14:15], -1, 0
	s_cmp_lg_u32 s12, s7
	s_cselect_b64 s[12:13], -1, 0
	s_and_b64 s[12:13], s[14:15], s[12:13]
	v_fmac_f32_e32 v83, 0x41d80000, v134
	v_fma_f32 v80, v134, s48, v98
	v_fma_f32 v81, v135, s49, v99
	s_and_b64 vcc, exec, s[12:13]
	s_cbranch_vccnz .LBB0_840
	s_mov_b32 s12, 0xc2000000
	s_mov_b32 s13, 0xc2040000
	v_add_f32_e32 v98, s12, v2
	v_add_f32_e32 v99, s13, v2
	s_movk_i32 s12, 0x200
	v_cmp_gt_u32_e32 vcc, s12, v188
	s_mov_b32 s12, -1.0
	s_mov_b32 s13, -2.0
	v_add_f32_e32 v188, s12, v2
	v_add_f32_e32 v189, s13, v2
	s_mov_b32 s12, 0xc2080000
	v_cndmask_b32_e32 v187, v161, v187, vcc
	s_mov_b32 s13, 0xc20c0000
	v_cmp_le_f32_e32 vcc, 0, v188
	v_cmp_gt_f32_e64 s[14:15], s82, v188
	v_add_f32_e32 v190, s12, v2
	v_add_f32_e32 v191, s13, v2
	v_cmp_le_f32_e64 s[12:13], 0, v189
	v_cmp_gt_f32_e64 s[16:17], s82, v189
	s_and_b64 vcc, vcc, s[14:15]
	v_cndmask_b32_e32 v185, v161, v185, vcc
	s_and_b64 vcc, s[12:13], s[16:17]
	s_mov_b32 s12, 0xc0400000
	s_mov_b32 s13, 0xc1000000
	v_add_f32_e32 v188, s12, v2
	v_add_f32_e32 v189, s13, v2
	s_mov_b32 s12, 0xc2200000
	v_cndmask_b32_e32 v186, v161, v186, vcc
	s_mov_b32 s13, 0xc2240000
	v_cmp_le_f32_e32 vcc, 0, v188
	v_cmp_gt_f32_e64 s[14:15], s82, v188
	v_add_f32_e32 v192, s12, v2
	v_add_f32_e32 v193, s13, v2
	v_cmp_le_f32_e64 s[12:13], 0, v189
	v_cmp_gt_f32_e64 s[16:17], s82, v189
	s_and_b64 vcc, vcc, s[14:15]
	v_cndmask_b32_e32 v86, v161, v86, vcc
	s_and_b64 vcc, s[12:13], s[16:17]
	s_mov_b32 s12, 0xc1100000
	s_mov_b32 s13, 0xc1200000
	v_add_f32_e32 v188, s12, v2
	v_add_f32_e32 v189, s13, v2
	s_mov_b32 s12, 0xc2280000
	v_cndmask_b32_e32 v87, v161, v87, vcc
	s_mov_b32 s13, 0xc22c0000
	v_cmp_le_f32_e32 vcc, 0, v188
	v_cmp_gt_f32_e64 s[14:15], s82, v188
	v_add_f32_e32 v196, s12, v2
	v_add_f32_e32 v197, s13, v2
	v_cmp_le_f32_e64 s[12:13], 0, v189
	v_cmp_gt_f32_e64 s[16:17], s82, v189
	s_and_b64 vcc, vcc, s[14:15]
	v_cndmask_b32_e32 v88, v161, v88, vcc
	s_and_b64 vcc, s[12:13], s[16:17]
	s_mov_b32 s12, 0xc1300000
	s_mov_b32 s13, 0xc1800000
	v_add_f32_e32 v188, s12, v2
	v_add_f32_e32 v189, s13, v2
	s_mov_b32 s12, 0xc2400000
	v_cndmask_b32_e32 v89, v161, v89, vcc
	s_mov_b32 s13, 0xc2440000
	v_cmp_le_f32_e32 vcc, 0, v188
	v_cmp_gt_f32_e64 s[14:15], s82, v188
	v_add_f32_e32 v198, s12, v2
	v_add_f32_e32 v199, s13, v2
	v_cmp_le_f32_e64 s[12:13], 0, v189
	v_cmp_gt_f32_e64 s[16:17], s82, v189
	s_and_b64 vcc, vcc, s[14:15]
	v_cndmask_b32_e32 v90, v161, v90, vcc
	s_and_b64 vcc, s[12:13], s[16:17]
	s_mov_b32 s12, 0xc1880000
	s_mov_b32 s13, 0xc1900000
	v_add_f32_e32 v188, s12, v2
	v_add_f32_e32 v189, s13, v2
	s_mov_b32 s12, 0xc2480000
	v_cndmask_b32_e32 v91, v161, v91, vcc
	s_mov_b32 s13, 0xc24c0000
	v_cmp_le_f32_e32 vcc, 0, v188
	v_cmp_gt_f32_e64 s[14:15], s82, v188
	v_add_f32_e32 v200, s12, v2
	v_add_f32_e32 v201, s13, v2
	v_cmp_le_f32_e64 s[12:13], 0, v189
	v_cmp_gt_f32_e64 s[16:17], s82, v189
	s_and_b64 vcc, vcc, s[14:15]
	v_cndmask_b32_e32 v92, v161, v92, vcc
	s_and_b64 vcc, s[12:13], s[16:17]
	s_mov_b32 s12, 0xc1980000
; template <int MODE> ...
;     ...
;         if (bcur >= bA || bcur == bB) {
;             const float base = (float)dist0;
; #pragma unroll
;             for (int r = 0; r < 16; ++r) { const float c0 = ks * (float)((r & 3) + 8 * (r >> 2)), c1 = c0 + 32.f * ks; const float d0 = base - c0, d1 = base - c1;
;                 bool v0 = d0 >= 0.f, v1 = d1 >= 0.f;
;                 if (MODE == 2) { v0 = v0 && (d0 < 512.f); v1 = v1 && (d1 < 512.f); }
;                 p0[r] = v0 ? p0[r] : -__builtin_inff(); p1[r] = v1 ? p1[r] : -__builtin_inff(); }
;         }
	s_mov_b32 s13, 0xc1c00000
	v_add_f32_e32 v188, s12, v2
	v_add_f32_e32 v189, s13, v2
	s_mov_b32 s12, 0xc2600000
	v_cndmask_b32_e32 v93, v161, v93, vcc
	s_mov_b32 s13, 0xc2640000
	v_cmp_le_f32_e32 vcc, 0, v188
	v_cmp_gt_f32_e64 s[14:15], s82, v188
	v_add_f32_e32 v202, s12, v2
	v_add_f32_e32 v203, s13, v2
	v_cmp_le_f32_e64 s[12:13], 0, v189
	v_cmp_gt_f32_e64 s[16:17], s82, v189
	s_and_b64 vcc, vcc, s[14:15]
	v_cndmask_b32_e32 v94, v161, v94, vcc
	s_and_b64 vcc, s[12:13], s[16:17]
	s_mov_b32 s12, 0xc1c80000
	s_mov_b32 s13, 0xc1d00000
	v_add_f32_e32 v188, s12, v2
	v_add_f32_e32 v189, s13, v2
	s_mov_b32 s12, 0xc2680000
	v_cndmask_b32_e32 v95, v161, v95, vcc
	s_mov_b32 s13, 0xc26c0000
	v_cmp_le_f32_e32 vcc, 0, v188
	v_cmp_gt_f32_e64 s[14:15], s82, v188
	v_add_f32_e32 v204, s12, v2
	v_add_f32_e32 v205, s13, v2
	v_cmp_le_f32_e64 s[12:13], 0, v189
	v_cmp_gt_f32_e64 s[16:17], s82, v189
	s_and_b64 vcc, vcc, s[14:15]
	v_cmp_le_f32_e64 s[14:15], 0, v190
	v_cmp_gt_f32_e64 s[48:49], s82, v190
	v_cndmask_b32_e32 v96, v161, v96, vcc
	s_and_b64 vcc, s[12:13], s[16:17]
	v_add_f32_e32 v82, 0xc1d80000, v2
	v_cmp_le_f32_e64 s[16:17], 0, v191
	v_cmp_gt_f32_e64 s[50:51], s82, v191
	s_and_b64 s[14:15], s[14:15], s[48:49]
	v_cndmask_b32_e32 v97, v161, v97, vcc
	v_cmp_le_f32_e32 vcc, 0, v82
	v_cmp_gt_f32_e64 s[12:13], s82, v82
	v_cmp_le_f32_e64 s[18:19], 0, v192
	v_cmp_gt_f32_e64 s[52:53], s82, v192
	v_cndmask_b32_e64 v84, v161, v84, s[14:15]
	s_and_b64 s[14:15], s[16:17], s[50:51]
	s_and_b64 vcc, vcc, s[12:13]
	v_cmp_le_f32_e64 s[20:21], 0, v193
	v_cmp_gt_f32_e64 s[54:55], s82, v193
	v_cndmask_b32_e64 v85, v161, v85, s[14:15]
	s_and_b64 s[14:15], s[18:19], s[52:53]
	v_cndmask_b32_e32 v83, v161, v83, vcc
	v_cmp_le_f32_e32 vcc, 0, v98
	v_cmp_le_f32_e64 s[22:23], 0, v196
	v_cmp_gt_f32_e64 s[44:45], s82, v98
	v_cmp_gt_f32_e64 s[56:57], s82, v196
	v_cndmask_b32_e64 v70, v161, v70, s[14:15]
	s_and_b64 s[14:15], s[20:21], s[54:55]
	v_cmp_le_f32_e64 s[24:25], 0, v197
	v_cmp_gt_f32_e64 s[58:59], s82, v197
	s_and_b64 vcc, vcc, s[44:45]
	v_cndmask_b32_e64 v71, v161, v71, s[14:15]
	s_and_b64 s[14:15], s[22:23], s[56:57]
	v_cmp_le_f32_e64 s[12:13], 0, v99
	v_cmp_le_f32_e64 s[26:27], 0, v198
	v_cmp_le_f32_e64 s[36:37], 0, v202
	v_cmp_gt_f32_e64 s[46:47], s82, v99
	v_cmp_gt_f32_e64 s[60:61], s82, v198
	v_cndmask_b32_e32 v68, v161, v68, vcc
	v_cmp_gt_f32_e32 vcc, s82, v202
	v_cndmask_b32_e64 v72, v161, v72, s[14:15]
	s_and_b64 s[14:15], s[24:25], s[58:59]
	v_cmp_le_f32_e64 s[28:29], 0, v199
	v_cmp_le_f32_e64 s[38:39], 0, v203
	v_cmp_gt_f32_e64 s[62:63], s82, v199
	s_and_b64 s[12:13], s[12:13], s[46:47]
	v_cmp_gt_f32_e64 s[46:47], s82, v203
	v_cndmask_b32_e64 v73, v161, v73, s[14:15]
	s_and_b64 s[14:15], s[26:27], s[60:61]
	s_and_b64 vcc, s[36:37], vcc
	v_cmp_le_f32_e64 s[30:31], 0, v200
	v_cmp_le_f32_e64 s[40:41], 0, v204
	v_cmp_gt_f32_e64 s[64:65], s82, v200
	v_cndmask_b32_e64 v69, v161, v69, s[12:13]
	v_cmp_gt_f32_e64 s[12:13], s82, v204
	v_cndmask_b32_e64 v74, v161, v74, s[14:15]
	s_and_b64 s[14:15], s[28:29], s[62:63]
	v_cndmask_b32_e32 v78, v161, v78, vcc
	s_and_b64 vcc, s[38:39], s[46:47]
	v_cmp_le_f32_e64 s[34:35], 0, v201
	v_cmp_le_f32_e64 s[42:43], 0, v205
	v_cmp_gt_f32_e64 s[44:45], s82, v201
	v_cmp_gt_f32_e64 s[48:49], s82, v205
	v_cndmask_b32_e64 v75, v161, v75, s[14:15]
	s_and_b64 s[14:15], s[30:31], s[64:65]
	v_cndmask_b32_e32 v79, v161, v79, vcc
	s_and_b64 vcc, s[40:41], s[12:13]
	v_readlane_b32 s50, v245, 61
	s_mov_b32 s56, 0x41000000
	s_mov_b32 s58, 0x44480000
	s_mov_b32 s60, 0x42000000
	s_mov_b32 s62, 0x43900000
	s_mov_b32 s64, 0
	v_cndmask_b32_e64 v76, v161, v76, s[14:15]
	s_and_b64 s[14:15], s[34:35], s[44:45]
	s_mov_b32 s44, 0x42600000
	s_mov_b32 s38, 0x41900000
	s_mov_b32 s36, 0x42280000
	s_mov_b32 s28, 0x41200000
	s_mov_b32 s26, 0x42200000
	s_mov_b32 s24, 0x42080000
	s_mov_b32 s22, 2.0
	s_mov_b32 s40, 0x42480000
	v_cndmask_b32_e32 v80, v161, v80, vcc
	s_and_b64 vcc, s[42:43], s[48:49]
	s_mov_b32 s48, 0x42680000
	s_mov_b32 s42, 0x41c00000
	v_readlane_b32 s51, v245, 62
	s_mov_b32 s57, 0x41100000
	s_mov_b32 s59, 0x444c0000
	s_mov_b32 s61, 0x42400000
	s_mov_b32 s63, 0x43980000
	v_readlane_b32 s31, v245, 58
	s_mov_b32 s65, 0x41800000
	s_mov_b32 s45, 0x42640000
	v_cndmask_b32_e64 v77, v161, v77, s[14:15]
	s_mov_b32 s46, 0x41d00000
	s_mov_b32 s39, 0x41980000
	s_mov_b32 s37, 0x422c0000
	s_mov_b32 s29, 0x41300000
	s_mov_b32 s27, 0x42240000
	s_mov_b32 s25, 0x420c0000
	s_mov_b32 s23, 0x40400000
	s_mov_b32 s41, 0x424c0000
	s_mov_b32 s49, 0x426c0000
	s_mov_b32 s43, 0x41c80000
	v_cndmask_b32_e32 v81, v161, v81, vcc
	s_mov_b32 s47, 0x41d80000
